# MoE expert-weight f32->fp8 conversion moved from phase 0 into the NSA tile loops (one 32x32 item per wave per tile iteration, loads waited one iteration later, DMA kept in flight); NSA PV/QK reorder d
# speedup vs baseline: 1.0149x; 1.0149x over previous
; #define LAS __attribute__((address_space(3)))
; __global__ void __launch_bounds__(512, 2) mk_fwd(Args a) {
;     extern __shared__ __attribute__((aligned(16))) unsigned char lds_raw[];
;     LAS unsigned char* lds = (LAS unsigned char*)lds_raw;
;     volatile LAS unsigned* MISC = (volatile LAS unsigned*)(lds + MISC_OFF);
;     if (threadIdx.x < 64) MISC[threadIdx.x] = 0u;
;     __syncthreads();
;     const int lo = a.ph_lo, hi = a.ph_hi;
;     ...
;     XcdBarrier bar = xcd_barrier_post((unsigned*)(a.ws + WS_CTL) + CW_BAR, MISC + 8);
_Z6mk_fwd4Args:
	s_load_dwordx8 s[60:67], s[0:1], 0xc0
	v_writelane_b32 v255, s2, 0
	s_load_dword s98, s[0:1], 0xf0
	s_and_b32 s99, s2, 7
	s_lshl_b32 s99, s99, 5
	s_lshr_b32 s100, s2, 3
	s_or_b32 s99, s99, s100
	s_waitcnt lgkmcnt(0)
	s_cmp_eq_u32 s98, 0x100
	s_cselect_b32 s99, s99, s2
	v_writelane_b32 v255, s99, 62
	s_load_dwordx2 s[98:99], s[0:1], 0xb8
	v_readfirstlane_b32 s100, v0
	s_lshr_b32 s100, s100, 6
	s_lshl_b32 s101, s2, 3
	s_add_u32 s100, s100, s101
	s_mov_b32 s101, 0
	s_waitcnt lgkmcnt(0)
	v_writelane_b32 v255, s0, 1
	s_load_dwordx2 s[4:5], s[0:1], 0xe0
	v_cmp_gt_u32_e32 vcc, 64, v0
	v_writelane_b32 v255, s1, 2
	s_and_saveexec_b64 s[0:1], vcc
	v_lshl_add_u32 v1, v0, 2, 0
	v_add_u32_e32 v1, 0x24400, v1
	v_mov_b32_e32 v2, 0
	ds_write_b32 v1, v2
	s_waitcnt lgkmcnt(0)
	v_writelane_b32 v255, s4, 3
	s_nop 1
	v_writelane_b32 v255, s5, 4
	s_or_b64 exec, exec, s[0:1]
	s_add_u32 s0, s66, 0x4000
	s_addc_u32 s1, s67, 0
	v_writelane_b32 v255, s0, 5
	s_barrier
	s_nop 0
	v_writelane_b32 v255, s1, 6
	s_getreg_b32 s0, hwreg(HW_REG_XCC_ID, 0, 4)
	s_and_b32 s0, s0, 15
	v_writelane_b32 v255, s0, 7
	v_cmp_ne_u32_e64 s[0:1], 0, v0
	v_cmp_eq_u32_e64 s[2:3], 0, v0
	s_nop 0
	v_writelane_b32 v255, s0, 8
	s_nop 1
	v_writelane_b32 v255, s1, 9
	s_mov_b64 s[0:1], exec
	v_writelane_b32 v255, s2, 10
	s_nop 1
	v_writelane_b32 v255, s3, 11
	s_and_b64 s[2:3], s[0:1], s[2:3]
	s_mov_b64 exec, s[2:3]
	s_cbranch_execz .LBB0_5
	s_mov_b64 s[2:3], exec
	v_mbcnt_lo_u32_b32 v1, s2, 0
	v_mbcnt_hi_u32_b32 v1, s3, v1
	v_cmp_eq_u32_e32 vcc, 0, v1
	s_and_b64 s[4:5], exec, vcc
	s_mov_b64 exec, s[4:5]
	s_cbranch_execz .LBB0_5
	v_readlane_b32 s4, v255, 7
	s_bcnt1_i32_b64 s2, s[2:3]
	s_lshl_b32 s4, s4, 8
	v_mov_b32_e32 v2, s2
	v_readlane_b32 s2, v255, 5
	v_mov_b32_e32 v1, s4
	v_readlane_b32 s3, v255, 6
	s_nop 4
	global_atomic_add v1, v2, s[2:3] offset:1024

; __device__ __forceinline__ void p0_weights(const Args& a, LAS unsigned char* lds) {
;     const int lane = threadIdx.x & 63, wave = __builtin_amdgcn_readfirstlane(threadIdx.x >> 6);
;     const int gw = blockIdx.x * 8 + wave, NGW = gridDim.x * 8;
;     constexpr int I_IN = 16 * 178, I_OUT = 16 * 64, I_FG = 16 * 176, I_FD = 44 * 64, I_MG = 16 * 224, I_MD = 56 * 64;
;     constexpr int NIT = 2 * I_IN + 2 * I_OUT + 2 * I_FG + I_FD + 16 * I_MG + 8 * I_MD;
;     auto decode = [&](int it) -> WItem {
;         WItem w; w.valid = false; w.src = nullptr; w.dst = nullptr; w.N = 0; w.K = 0; w.k0 = 0; w.n = 0; w.kind = 0; w.f8 = false; w.scale = 1.f;
;         if (it >= NIT) return w;
;         int r = it; const float* W;
;         if (r < 2 * I_IN) { const int l = r / I_IN; r -= l * I_IN; W = a.in[I_WIN] + (size_t)l * D * INW; w.K = D; w.N = INW; w.dst = a.ws + WS_WIN_T + (size_t)l * PW * D * 2; w.kind = 1; }
;         else if ((r -= 2 * I_IN) < 2 * I_OUT) { const int l = r / I_OUT; r -= l * I_OUT; W = a.in[I_WOUT] + (size_t)l * D * D; w.K = D; w.N = D; w.dst = a.ws + WS_WOUT_T + (size_t)l * D * D * 2; }
;         else if ((r -= 2 * I_OUT) < 2 * I_FG) { const int up = r / I_FG; r -= up * I_FG; W = a.in[up ? I_FWU : I_FWG]; w.K = D; w.N = DFF; w.dst = a.ws + WS_FGU_T; w.kind = 2 + up; w.f8 = FFN8_GU; w.scale = F8_WGU; }
;         else if ((r -= 2 * I_FG) < I_FD) { W = a.in[I_FWD]; w.K = DFF; w.N = D; w.dst = a.ws + WS_FD_T; w.f8 = FFN8_DN; w.scale = F8_FD; }
;         else if ((r -= I_FD) < 16 * I_MG) { const int up = r / (8 * I_MG); r -= up * 8 * I_MG; const int e = r / I_MG; r -= e * I_MG; W = a.in[up ? I_MWU : I_MWG] + (size_t)e * D * DFE; w.K = D; w.N = DFE;
;             w.dst = a.ws + WS_MGU_T + (size_t)e * 2 * DFE * D * (MOE_FP8 ? 1 : 2); w.kind = 2 + up; w.f8 = MOE_FP8; w.scale = F8_WGU; }
;         else { r -= 16 * I_MG; const int e = r / I_MD; r -= e * I_MD; W = a.in[I_MWD] + (size_t)e * DFE * D; w.K = DFE; w.N = D; w.dst = a.ws + WS_MD_T + (size_t)e * D * DFE * (MOE_FP8 ? 1 : 2); w.f8 = MOE_FP8; w.scale = F8_WD; }
;         const int nblk = (w.N + 31) >> 5, kb = r / nblk, nb = r - kb * nblk;
;         w.k0 = 128 * kb + 16 * (lane >> 3); w.n = 32 * nb + 4 * (lane & 7); w.valid = w.n < w.N; w.src = W + (size_t)w.k0 * w.N + w.n;
;         return w;
;     };
;     { f32x4 v[16], vn[16];
;       WItem cur = decode(gw); witem_load(cur, v);
; #pragma unroll 1
.LBB0_18:
	s_or_b64 exec, exec, s[0:1]
	v_readfirstlane_b32 s0, v0
	s_lshr_b32 s14, s0, 6
	v_readlane_b32 s0, v255, 0
	s_lshl_b32 s31, s0, 3
	s_add_i32 s34, s14, s31
	s_cmp_gt_i32 s34, 0x3f3f
	s_cbranch_scc1 .LBB0_25
	s_cmpk_gt_i32 s34, 0x163f
	s_cbranch_scc0 .LBB0_26
	s_cmpk_gt_u32 s34, 0x1e3f
	s_mov_b64 s[0:1], -1
	s_cbranch_scc0 .LBB0_27
	s_cmpk_gt_u32 s34, 0x343f
	s_cbranch_scc0 .LBB0_28
	s_cmpk_gt_u32 s34, 0x3f3f
	s_cbranch_scc0 .LBB0_29
	s_cmp_gt_u32 s34, 0x11f3f
	s_cbranch_scc0 .LBB0_30
	s_add_i32 s2, s34, 0xfffee0c0
	s_bfe_u32 s3, s2, 0x100009
	s_mulk_i32 s3, 0x2493
	s_lshr_b32 s3, s3, 16
	s_mul_i32 s4, s3, 0xfffff200
	s_add_i32 s15, s4, s2
	s_mul_i32 s2, s3, 0x3800000
	s_add_u32 s6, s62, s2
	s_addc_u32 s7, s63, 0
	s_mul_i32 s3, s3, 0xe00000
	s_add_u32 s2, s66, s3
	s_addc_u32 s3, s67, 0
	s_add_u32 s4, s2, 0x66000000
	s_addc_u32 s5, s3, 0
	s_mov_b64 s[2:3], 0
	s_branch .LBB0_31

; __device__ __forceinline__ void p0_weights(const Args& a, LAS unsigned char* lds) {
;     ...
;     { f32x4 v[16], vn[16];
;       WItem cur = decode(gw); witem_load(cur, v);
; #pragma unroll 1
;       for (int it = gw; it < NIT; it += NGW) {
;           const WItem nxt = decode(it + NGW); witem_load(nxt, vn);
.LBB0_46:
	s_or_b64 exec, exec, s[6:7]
	s_waitcnt lgkmcnt(0)
	s_lshl_b32 s30, s28, 3
	s_cmp_gt_i32 s34, 0x3f3f
	s_cbranch_scc1 .LBB0_268
	s_add_u32 s2, s66, 0x66000000
	v_writelane_b32 v255, s2, 54
	s_addc_u32 s2, s67, 0
	s_add_u32 s37, s66, 0x4a000000
	s_addc_u32 s38, s67, 0
	s_add_u32 s6, s66, 0x48a00000
	s_addc_u32 s7, s67, 0
	s_add_u32 s10, s66, 0x45e00000
	s_addc_u32 s11, s67, 0
	s_add_u32 s39, s66, 0x44e00000
	s_addc_u32 s40, s67, 0
	s_add_u32 s41, s66, 0x42000000
	v_writelane_b32 v255, s2, 56
	s_addc_u32 s42, s67, 0
	s_add_i32 s2, s31, s30
	v_lshlrev_b32_e32 v66, 1, v0
	s_add_i32 s2, s2, s14
	v_and_b32_e32 v136, 0x70, v66
	v_and_b32_e32 v137, 28, v142
	s_add_i32 s43, s30, 0xfffee0c0
	s_add_i32 s68, s2, 0xe0c0
	s_mov_b32 s13, 0
	s_movk_i32 s69, 0xff00
	s_movk_i32 s70, 0x80
	s_movk_i32 s71, 0x9ff
	s_movk_i32 s72, 0xa17
	s_movk_i32 s75, 0x7fff
	s_mov_b32 s76, 0xffff0000
	s_movk_i32 s77, 0x9fe
	s_movk_i32 s78, 0xa16
	s_movk_i32 s97, 0x9fd
	s_movk_i32 s74, 0xa15
	s_movk_i32 s73, 0x9fc
	s_movk_i32 s79, 0xa14
	s_branch .LBB0_53

; __device__ __forceinline__ void p0_weights(const Args& a, LAS unsigned char* lds) {
;     ...
;     auto decode = [&](int it) -> WItem {
;         WItem w; w.valid = false; w.src = nullptr; w.dst = nullptr; w.N = 0; w.K = 0; w.k0 = 0; w.n = 0; w.kind = 0; w.f8 = false; w.scale = 1.f;
;         if (it >= NIT) return w;
;         int r = it; const float* W;
;         if (r < 2 * I_IN) { const int l = r / I_IN; r -= l * I_IN; W = a.in[I_WIN] + (size_t)l * D * INW; w.K = D; w.N = INW; w.dst = a.ws + WS_WIN_T + (size_t)l * PW * D * 2; w.kind = 1; }
;         else if ((r -= 2 * I_IN) < 2 * I_OUT) { const int l = r / I_OUT; r -= l * I_OUT; W = a.in[I_WOUT] + (size_t)l * D * D; w.K = D; w.N = D; w.dst = a.ws + WS_WOUT_T + (size_t)l * D * D * 2; }
;         else if ((r -= 2 * I_OUT) < 2 * I_FG) { const int up = r / I_FG; r -= up * I_FG; W = a.in[up ? I_FWU : I_FWG]; w.K = D; w.N = DFF; w.dst = a.ws + WS_FGU_T; w.kind = 2 + up; w.f8 = FFN8_GU; w.scale = F8_WGU; }
;         else if ((r -= 2 * I_FG) < I_FD) { W = a.in[I_FWD]; w.K = DFF; w.N = D; w.dst = a.ws + WS_FD_T; w.f8 = FFN8_DN; w.scale = F8_FD; }
;         else if ((r -= I_FD) < 16 * I_MG) { const int up = r / (8 * I_MG); r -= up * 8 * I_MG; const int e = r / I_MG; r -= e * I_MG; W = a.in[up ? I_MWU : I_MWG] + (size_t)e * D * DFE; w.K = D; w.N = DFE;
;             w.dst = a.ws + WS_MGU_T + (size_t)e * 2 * DFE * D * (MOE_FP8 ? 1 : 2); w.kind = 2 + up; w.f8 = MOE_FP8; w.scale = F8_WGU; }
;         else { r -= 16 * I_MG; const int e = r / I_MD; r -= e * I_MD; W = a.in[I_MWD] + (size_t)e * DFE * D; w.K = DFE; w.N = D; w.dst = a.ws + WS_MD_T + (size_t)e * D * DFE * (MOE_FP8 ? 1 : 2); w.f8 = MOE_FP8; w.scale = F8_WD; }
;     ...
;       WItem cur = decode(gw); witem_load(cur, v);
; #pragma unroll 1
;       for (int it = gw; it < NIT; it += NGW) {
;           const WItem nxt = decode(it + NGW); witem_load(nxt, vn);
;           __builtin_amdgcn_sched_barrier(0);
;           witem_store(cur, v);
;           __builtin_amdgcn_sched_barrier(0);
; #pragma unroll
;           for (int i = 0; i < 16; ++i) v[i] = vn[i];
;           cur = nxt; } }
.LBB0_52:
	s_or_b64 exec, exec, s[18:19]
	s_add_i32 s68, s68, s30
	s_cmp_gt_i32 s34, 0x3f3f
	s_cbranch_scc1 .LBB0_268
.LBB0_53:
	s_mov_b32 s12, s34
	s_waitcnt vmcnt(15)
	v_mov_b64_e32 v[128:129], v[4:5]
	s_waitcnt vmcnt(14)
	v_mov_b64_e32 v[124:125], v[8:9]
	s_waitcnt vmcnt(13)
	v_mov_b64_e32 v[120:121], v[12:13]
	s_waitcnt vmcnt(12)
	v_mov_b64_e32 v[116:117], v[16:17]
	s_waitcnt vmcnt(11)
	v_mov_b64_e32 v[112:113], v[20:21]
	s_waitcnt vmcnt(10)
	v_mov_b64_e32 v[108:109], v[24:25]
	s_waitcnt vmcnt(9)
	v_mov_b64_e32 v[104:105], v[28:29]
	s_waitcnt vmcnt(8)
	v_mov_b64_e32 v[100:101], v[32:33]
	s_waitcnt vmcnt(7)
	v_mov_b64_e32 v[96:97], v[36:37]
	s_waitcnt vmcnt(6)
	v_mov_b64_e32 v[92:93], v[40:41]
	s_waitcnt vmcnt(5)
	v_mov_b64_e32 v[88:89], v[44:45]
	s_waitcnt vmcnt(4)
	v_mov_b64_e32 v[84:85], v[48:49]
	s_waitcnt vmcnt(3)
	v_mov_b64_e32 v[80:81], v[52:53]
	s_waitcnt vmcnt(2)
	v_mov_b64_e32 v[76:77], v[56:57]
	s_waitcnt vmcnt(1)
	v_mov_b64_e32 v[68:69], v[60:61]
	s_add_i32 s34, s34, s30
	s_waitcnt vmcnt(0)
	v_mov_b64_e32 v[72:73], v[64:65]
	s_mov_b64 s[14:15], s[4:5]
	s_mov_b32 s33, s96
	v_mov_b32_e32 v130, v139
	v_mov_b32_e32 v138, v132
	s_mov_b32 s36, s3
	s_mov_b64 s[18:19], s[0:1]
	s_mov_b64 s[20:21], s[16:17]
	s_mov_b32 s2, s35
	v_mov_b64_e32 v[126:127], v[2:3]
	v_mov_b64_e32 v[122:123], v[6:7]
	v_mov_b64_e32 v[118:119], v[10:11]
	v_mov_b64_e32 v[114:115], v[14:15]
	v_mov_b64_e32 v[110:111], v[18:19]
	v_mov_b64_e32 v[106:107], v[22:23]
	v_mov_b64_e32 v[102:103], v[26:27]
	v_mov_b64_e32 v[98:99], v[30:31]
	v_mov_b64_e32 v[94:95], v[34:35]
	v_mov_b64_e32 v[90:91], v[38:39]
	v_mov_b64_e32 v[86:87], v[42:43]
	v_mov_b64_e32 v[82:83], v[46:47]
	v_mov_b64_e32 v[78:79], v[50:51]
	v_mov_b64_e32 v[74:75], v[54:55]
	v_mov_b64_e32 v[66:67], v[58:59]
	s_cmp_gt_i32 s34, 0x3f3f
	v_mov_b64_e32 v[70:71], v[62:63]
	s_cbranch_scc1 .LBB0_62
	s_cmpk_gt_i32 s34, 0x163f
	s_mov_b64 s[16:17], -1
	s_cbranch_scc0 .LBB0_72
	s_mov_b64 s[0:1], -1
	s_cmpk_gt_u32 s34, 0x1e3f
	s_cbranch_scc0 .LBB0_69
	s_cmpk_gt_u32 s34, 0x343f
	s_cbranch_scc0 .LBB0_66
	s_cmpk_gt_u32 s34, 0x3f3f
	s_cbranch_scc0 .LBB0_63
	s_cmp_gt_u32 s34, 0x11f3f
	s_cbranch_scc0 .LBB0_60
	s_add_i32 s4, s34, 0xe0c0
	s_and_b32 s3, 0xffff, s68
	s_bfe_u32 s4, s4, 0x70009
	s_mul_hi_u32 s3, s3, 0x124925
	s_mulk_i32 s4, 0x2493
	s_mulk_i32 s3, 0xf200
	s_lshr_b32 s4, s4, 16
	s_add_i32 s5, s43, s12
	s_add_i32 s24, s5, s3
	s_mul_i32 s3, s4, 0x3800000
	s_add_u32 s22, s62, s3
	s_addc_u32 s23, s63, 0
	s_mul_i32 s4, s4, 0xe00000
	v_readlane_b32 s3, v255, 54
	s_add_u32 s4, s3, s4
	v_readlane_b32 s3, v255, 56
	s_addc_u32 s5, s3, 0
	s_mov_b64 s[16:17], 0

; __device__ __forceinline__ void p0_weights(const Args& a, LAS unsigned char* lds) {
;     ...
;         else if ((r -= I_FD) < 16 * I_MG) { const int up = r / (8 * I_MG); r -= up * 8 * I_MG; const int e = r / I_MG; r -= e * I_MG; W = a.in[up ? I_MWU : I_MWG] + (size_t)e * D * DFE; w.K = D; w.N = DFE;
;             w.dst = a.ws + WS_MGU_T + (size_t)e * 2 * DFE * D * (MOE_FP8 ? 1 : 2); w.kind = 2 + up; w.f8 = MOE_FP8; w.scale = F8_WGU; }
;         else { r -= 16 * I_MG; const int e = r / I_MD; r -= e * I_MD; W = a.in[I_MWD] + (size_t)e * DFE * D; w.K = DFE; w.N = D; w.dst = a.ws + WS_MD_T + (size_t)e * D * DFE * (MOE_FP8 ? 1 : 2); w.f8 = MOE_FP8; w.scale = F8_WD; }
;         const int nblk = (w.N + 31) >> 5, kb = r / nblk, nb = r - kb * nblk;
;         w.k0 = 128 * kb + 16 * (lane >> 3); w.n = 32 * nb + 4 * (lane & 7); w.valid = w.n < w.N; w.src = W + (size_t)w.k0 * w.N + w.n;
; __device__ __forceinline__ void nsa_unit(const Args& a, LAS unsigned char* lds, int b, int kvh, int qb) {
;     ...
; #pragma unroll
;     for (int dt = 0; dt < 4; ++dt)
; #pragma unroll
;         for (int i = 0; i < 16; ++i) o[dt][i] = 0.f;
;     float mrun = -1e30f, lrun = 0.f;
;     f32x16 p0, p1;
; #pragma unroll
;     for (int i = 0; i < 16; ++i) { p0[i] = 0.f; p1[i] = 0.f; }
;     bf16x8 pf[2][2];
;     if (w >= 4) asm volatile("s_barrier" ::: "memory");
; #pragma unroll 1
;     for (int it = 0; it <= nTot; ++it) {
.LBB0_894:
	s_cmp_lt_i32 s15, -1
	s_cbranch_scc1 .LBB0_919
	v_mov_b32_e32 v49, v47
	s_lshl_b32 s0, s72, 1
	s_max_i32 s1, s72, 8
	v_mov_b32_e32 v60, v47
	v_mov_b32_e32 v61, v47
	v_lshl_add_u64 v[206:207], s[30:31], 0, v[48:49]
	s_sub_i32 s63, s0, s1
	v_mov_b32_e32 v46, v47
	v_mov_b32_e32 v48, v47
	v_mov_b32_e32 v50, v47
	v_mov_b32_e32 v51, v47
	v_mov_b32_e32 v52, v47
	v_mov_b32_e32 v53, v47
	v_mov_b32_e32 v54, v47
	v_mov_b32_e32 v55, v47
	v_mov_b32_e32 v56, v47
	v_mov_b32_e32 v57, v47
	v_mov_b32_e32 v58, v47
	v_mov_b32_e32 v59, v47
	v_mov_b64_e32 v[108:109], v[60:61]
	v_mov_b64_e32 v[124:125], v[60:61]
	v_mov_b64_e32 v[140:141], v[60:61]
	v_mov_b64_e32 v[156:157], v[60:61]
	v_mov_b64_e32 v[76:77], v[60:61]
	v_mov_b64_e32 v[92:93], v[60:61]
	v_add_u32_e32 v43, 1, v249
	s_add_i32 s23, s63, 11
	s_add_i32 s24, s63, 10
	s_mov_b32 s62, 2
	s_add_i32 s63, s63, 2
	s_mov_b32 s74, 0
	v_mov_b32_e32 v208, 0xf149f2ca
	v_mov_b32_e32 v209, 0
	s_movk_i32 s75, 0xc000
	v_mov_b64_e32 v[106:107], v[58:59]
	v_mov_b64_e32 v[104:105], v[56:57]
	v_mov_b64_e32 v[102:103], v[54:55]
	v_mov_b64_e32 v[100:101], v[52:53]
	v_mov_b64_e32 v[98:99], v[50:51]
	v_mov_b64_e32 v[96:97], v[48:49]
	v_mov_b64_e32 v[94:95], v[46:47]
	v_mov_b64_e32 v[122:123], v[58:59]
	v_mov_b64_e32 v[120:121], v[56:57]
	v_mov_b64_e32 v[118:119], v[54:55]
	v_mov_b64_e32 v[116:117], v[52:53]
	v_mov_b64_e32 v[114:115], v[50:51]
	v_mov_b64_e32 v[112:113], v[48:49]
	v_mov_b64_e32 v[110:111], v[46:47]
	v_mov_b64_e32 v[138:139], v[58:59]
	v_mov_b64_e32 v[136:137], v[56:57]
	v_mov_b64_e32 v[134:135], v[54:55]
	v_mov_b64_e32 v[132:133], v[52:53]
	v_mov_b64_e32 v[130:131], v[50:51]
	v_mov_b64_e32 v[128:129], v[48:49]
	v_mov_b64_e32 v[126:127], v[46:47]
	v_mov_b64_e32 v[154:155], v[58:59]
	v_mov_b64_e32 v[152:153], v[56:57]
	v_mov_b64_e32 v[150:151], v[54:55]
	v_mov_b64_e32 v[148:149], v[52:53]
	v_mov_b64_e32 v[146:147], v[50:51]
	v_mov_b64_e32 v[144:145], v[48:49]
	v_mov_b64_e32 v[142:143], v[46:47]
	v_mov_b64_e32 v[74:75], v[58:59]
	v_mov_b64_e32 v[72:73], v[56:57]
	v_mov_b64_e32 v[70:71], v[54:55]
	v_mov_b64_e32 v[68:69], v[52:53]
	v_mov_b64_e32 v[66:67], v[50:51]
	v_mov_b64_e32 v[64:65], v[48:49]
	v_mov_b64_e32 v[62:63], v[46:47]
	v_mov_b64_e32 v[90:91], v[58:59]
	v_mov_b64_e32 v[88:89], v[56:57]
	v_mov_b64_e32 v[86:87], v[54:55]
	v_mov_b64_e32 v[84:85], v[52:53]
	v_mov_b64_e32 v[82:83], v[50:51]
	v_mov_b64_e32 v[80:81], v[48:49]
	v_mov_b64_e32 v[78:79], v[46:47]
	s_waitcnt vmcnt(0)
	s_and_b32 s12, s101, 0x7fffffff
	s_cmp_ge_u32 s12, 168
	s_cbranch_scc1 .Lcn_ldum_n0s
	s_and_b32 s12, s101, 0x7fffffff
	s_mul_i32 s13, s12, 0x2493
	s_lshr_b32 s13, s13, 16
	s_mul_i32 s65, s13, 7
	s_sub_u32 s65, s12, s65
	s_lshl_b32 s65, s65, 11
	s_add_u32 s65, s65, s100
	s_cmp_ge_u32 s13, 16
	s_cbranch_scc1 .Lcn_dn_n0ss
	s_lshr_b32 s66, s65, 5
	s_mul_i32 s66, s66, 0x2493
	s_lshr_b32 s66, s66, 16
	s_mul_i32 s67, s66, 0xe0
	s_sub_u32 s67, s65, s67
	s_and_b32 s65, s13, 1
	s_lshr_b32 s13, s13, 1
	s_mul_i32 s12, s13, 0x3800000
	s_mul_i32 s13, s66, 0xe0000
	s_add_u32 s12, s12, s13
	s_lshl_b32 s13, s67, 7
	s_add_u32 s12, s12, s13
	v_readlane_b32 s32, v255, 46
	v_readlane_b32 s33, v255, 47
	s_cmp_eq_u32 s65, 0
	s_cselect_b32 s32, s98, s32
	s_cselect_b32 s33, s99, s33
	s_add_u32 s32, s32, s12
	s_addc_u32 s33, s33, 0
	s_mov_b32 s1, 1
	s_branch .Lcn_dd_n0ss
.Lcn_dn_n0ss:
	s_sub_u32 s13, s13, 16
	s_lshr_b32 s66, s65, 6
	s_and_b32 s67, s65, 63
	s_mul_i32 s12, s13, 0x3800000
	s_lshl_b32 s13, s66, 18
	s_add_u32 s12, s12, s13
	s_lshl_b32 s13, s67, 7
	s_add_u32 s12, s12, s13
	v_readlane_b32 s32, v255, 48
	v_readlane_b32 s33, v255, 49
	s_add_u32 s32, s32, s12
	s_addc_u32 s33, s33, 0
	s_mov_b32 s1, 2
.Lcn_dd_n0ss:
	s_add_u32 s101, s101, 1
	s_bitset1_b32 s101, 31
	s_branch .Lcn_lgo_n0s
.Lcn_ldum_n0s:
	v_readlane_b32 s32, v255, 52
	v_readlane_b32 s33, v255, 53
	s_add_u32 s32, s32, 0x500000
	s_addc_u32 s33, s33, 0
	s_mov_b32 s1, 2
.Lcn_lgo_n0s:
	s_movk_i32 s12, 0x2000
	s_cmp_eq_u32 s1, 1
	s_cselect_b32 s12, 0x7000, s12
	v_and_b32_e32 v224, 63, v0
	v_and_b32_e32 v253, 7, v224
	v_lshrrev_b32_e32 v224, 3, v224
	v_lshlrev_b32_e32 v224, 2, v224
	v_lshlrev_b32_e32 v225, 4, v253
	v_lshlrev_b32_e32 v253, 2, v253
	v_mad_u32_u24 v254, v224, s12, v225
	global_load_dwordx4 v[212:215], v254, s[32:33] nt
	s_add_u32 s32, s32, s12
	s_addc_u32 s33, s33, 0
	global_load_dwordx4 v[216:219], v254, s[32:33] nt
	s_add_u32 s32, s32, s12
	s_addc_u32 s33, s33, 0
	global_load_dwordx4 v[220:223], v254, s[32:33] nt
	s_add_u32 s32, s32, s12
	s_addc_u32 s33, s33, 0
	global_load_dwordx2 v[224:225], v254, s[32:33] offset:0 nt
	global_load_dword v253, v254, s[32:33] offset:8 nt
	global_load_dword v254, v254, s[32:33] offset:12 nt
	s_branch .LBB0_897
.LBB0_896:
	s_add_i32 s12, s74, 2
	s_cmp_gt_i32 s12, s15
	s_cbranch_scc1 .Lcn_w0_n0
	s_waitcnt vmcnt(4)
	s_branch .Lcn_wd_n0

; __device__ __forceinline__ unsigned pk4_fp8(float a, float b, float c, float d) { int p = __builtin_amdgcn_cvt_pk_fp8_f32(a, b, 0, false); p = __builtin_amdgcn_cvt_pk_fp8_f32(c, d, p, true); return (unsigned)p; }
; __device__ __forceinline__ int witem_row(int kind, int n) {
;     if (kind == 1) return inproj_dst_row(n);
;     if (kind == 2) return ((n >> 7) << 8) + (n & 127);
;     if (kind == 3) return ((n >> 7) << 8) + 128 + (n & 127);
;     return n;
; }
; __device__ __forceinline__ void witem_load(const WItem& w, f32x4 (&v)[16]) {
;     if (!w.valid) return;
; #pragma unroll
;     for (int i = 0; i < 16; ++i) v[i] = *(const f32x4*)(w.src + (size_t)i * w.N);
; }
; __device__ __forceinline__ void witem_store(const WItem& w, const f32x4 (&v)[16]) {
;     if (!w.valid) return;
;     if (w.f8) {
; #pragma unroll
;         for (int j = 0; j < 4; ++j) { u32x4 o; const float sc = w.scale;
;             o.x = pk4_fp8(v[0][j] * sc, v[1][j] * sc, v[2][j] * sc, v[3][j] * sc); o.y = pk4_fp8(v[4][j] * sc, v[5][j] * sc, v[6][j] * sc, v[7][j] * sc);
;             o.z = pk4_fp8(v[8][j] * sc, v[9][j] * sc, v[10][j] * sc, v[11][j] * sc); o.w = pk4_fp8(v[12][j] * sc, v[13][j] * sc, v[14][j] * sc, v[15][j] * sc);
;             *(u32x4*)(w.dst + (size_t)witem_row(w.kind, w.n + j) * w.K + w.k0) = o; }
; __device__ __forceinline__ void p0_weights(const Args& a, LAS unsigned char* lds) {
;     ...
;         else if ((r -= I_FD) < 16 * I_MG) { const int up = r / (8 * I_MG); r -= up * 8 * I_MG; const int e = r / I_MG; r -= e * I_MG; W = a.in[up ? I_MWU : I_MWG] + (size_t)e * D * DFE; w.K = D; w.N = DFE;
;             w.dst = a.ws + WS_MGU_T + (size_t)e * 2 * DFE * D * (MOE_FP8 ? 1 : 2); w.kind = 2 + up; w.f8 = MOE_FP8; w.scale = F8_WGU; }
;         else { r -= 16 * I_MG; const int e = r / I_MD; r -= e * I_MD; W = a.in[I_MWD] + (size_t)e * DFE * D; w.K = DFE; w.N = D; w.dst = a.ws + WS_MD_T + (size_t)e * D * DFE * (MOE_FP8 ? 1 : 2); w.f8 = MOE_FP8; w.scale = F8_WD; }
;         const int nblk = (w.N + 31) >> 5, kb = r / nblk, nb = r - kb * nblk;
;         w.k0 = 128 * kb + 16 * (lane >> 3); w.n = 32 * nb + 4 * (lane & 7); w.valid = w.n < w.N; w.src = W + (size_t)w.k0 * w.N + w.n;
.Lcn_wd_n0:
	s_bitcmp1_b32 s101, 31
	s_cbranch_scc0 .Lcn_snone_n0l
	s_and_b32 s12, s101, 0x7fffffff
	s_sub_u32 s12, s12, 1
	s_mul_i32 s13, s12, 0x2493
	s_lshr_b32 s13, s13, 16
	s_mul_i32 s65, s13, 7
	s_sub_u32 s65, s12, s65
	s_lshl_b32 s65, s65, 11
	s_add_u32 s65, s65, s100
	s_cmp_ge_u32 s13, 16
	s_cbranch_scc1 .Lcn_dn_n0ld
	s_lshr_b32 s66, s65, 5
	s_mul_i32 s66, s66, 0x2493
	s_lshr_b32 s66, s66, 16
	s_mul_i32 s67, s66, 0xe0
	s_sub_u32 s67, s65, s67
	s_and_b32 s65, s13, 1
	s_lshr_b32 s13, s13, 1
	s_mul_i32 s12, s13, 0x1c00000
	s_add_u32 s12, s12, 0x4a000000
	s_lshr_b32 s13, s67, 2
	s_lshl_b32 s13, s13, 8
	s_lshl_b32 s65, s65, 7
	s_add_u32 s13, s13, s65
	s_and_b32 s65, s67, 3
	s_lshl_b32 s65, s65, 5
	s_add_u32 s13, s13, s65
	s_lshl_b32 s13, s13, 11
	s_add_u32 s12, s12, s13
	s_lshl_b32 s13, s66, 5
	s_add_u32 s12, s12, s13
	v_readlane_b32 s32, v255, 52
	v_readlane_b32 s33, v255, 53
	s_add_u32 s32, s32, s12
	s_addc_u32 s33, s33, 0
	s_mov_b32 s1, 1
	s_branch .Lcn_dd_n0ld
.Lcn_dn_n0ld:
	s_sub_u32 s13, s13, 16
	s_lshr_b32 s66, s65, 6
	s_and_b32 s67, s65, 63
	s_mul_i32 s12, s13, 0xe00000
	s_add_u32 s12, s12, 0x66000000
	s_mul_i32 s13, s67, 0x38000
	s_add_u32 s12, s12, s13
	s_lshl_b32 s13, s66, 5
	s_add_u32 s12, s12, s13
	v_readlane_b32 s32, v255, 52
	v_readlane_b32 s33, v255, 53
	s_add_u32 s32, s32, s12
	s_addc_u32 s33, s33, 0
	s_mov_b32 s1, 2
.Lcn_dd_n0ld:
	s_bitset0_b32 s101, 31
	s_mov_b32 s0, 0x42000000
	s_movk_i32 s12, 0x800
	s_cmp_eq_u32 s1, 2
	s_cselect_b32 s0, 0x43000000, s0
	s_cselect_b32 s12, 0x1c00, s12
	v_mul_f32_e32 v212, s0, v212
	v_mul_f32_e32 v213, s0, v213
	v_mul_f32_e32 v214, s0, v214
	v_mul_f32_e32 v215, s0, v215
	v_mul_f32_e32 v216, s0, v216
	v_mul_f32_e32 v217, s0, v217
	v_mul_f32_e32 v218, s0, v218
	v_mul_f32_e32 v219, s0, v219
	v_mul_f32_e32 v220, s0, v220
	v_mul_f32_e32 v221, s0, v221
	v_mul_f32_e32 v222, s0, v222
	v_mul_f32_e32 v223, s0, v223
	v_mul_f32_e32 v224, s0, v224
	v_mul_f32_e32 v225, s0, v225
	v_mul_f32_e32 v253, s0, v253
	v_mul_f32_e32 v254, s0, v254
	v_cvt_pk_fp8_f32 v212, v212, v216
	v_cvt_pk_fp8_f32 v213, v213, v217
	v_cvt_pk_fp8_f32 v214, v214, v218
	v_cvt_pk_fp8_f32 v215, v215, v219
	v_cvt_pk_fp8_f32 v212, v220, v224 op_sel:[0,0,1]
	v_cvt_pk_fp8_f32 v213, v221, v225 op_sel:[0,0,1]
	v_cvt_pk_fp8_f32 v214, v222, v253 op_sel:[0,0,1]
	v_cvt_pk_fp8_f32 v215, v223, v254 op_sel:[0,0,1]
	v_and_b32_e32 v216, 63, v0
	v_and_b32_e32 v218, 7, v216
	v_lshrrev_b32_e32 v216, 3, v216
	v_lshlrev_b32_e32 v216, 2, v216
	v_lshlrev_b32_e32 v217, 4, v218
	v_lshlrev_b32_e32 v218, 2, v218
	v_mad_u32_u24 v217, v218, s12, v216
	global_store_dword v217, v212, s[32:33] nt
	v_add_u32_e32 v216, s12, v217
	global_store_dword v216, v213, s[32:33] nt
	v_add_u32_e32 v218, s12, v216
	global_store_dword v218, v214, s[32:33] nt
	v_add_u32_e32 v219, s12, v218
	global_store_dword v219, v215, s[32:33] nt
.Lcn_snone_n0l:
	s_and_b32 s12, s101, 0x7fffffff
	s_cmp_ge_u32 s12, 168
	s_cbranch_scc1 .Lcn_ldum_n0l
	s_and_b32 s12, s101, 0x7fffffff
	s_mul_i32 s13, s12, 0x2493
	s_lshr_b32 s13, s13, 16
	s_mul_i32 s65, s13, 7
	s_sub_u32 s65, s12, s65
	s_lshl_b32 s65, s65, 11
	s_add_u32 s65, s65, s100
	s_cmp_ge_u32 s13, 16
	s_cbranch_scc1 .Lcn_dn_n0ls
	s_lshr_b32 s66, s65, 5
	s_mul_i32 s66, s66, 0x2493
	s_lshr_b32 s66, s66, 16
	s_mul_i32 s67, s66, 0xe0
	s_sub_u32 s67, s65, s67
	s_and_b32 s65, s13, 1
	s_lshr_b32 s13, s13, 1
	s_mul_i32 s12, s13, 0x3800000
	s_mul_i32 s13, s66, 0xe0000
	s_add_u32 s12, s12, s13
	s_lshl_b32 s13, s67, 7
	s_add_u32 s12, s12, s13
	v_readlane_b32 s32, v255, 46
	v_readlane_b32 s33, v255, 47
	s_cmp_eq_u32 s65, 0
	s_cselect_b32 s32, s98, s32
	s_cselect_b32 s33, s99, s33
	s_add_u32 s32, s32, s12
	s_addc_u32 s33, s33, 0
	s_mov_b32 s1, 1
	s_branch .Lcn_dd_n0ls

; __device__ __forceinline__ void witem_load(const WItem& w, f32x4 (&v)[16]) {
;     if (!w.valid) return;
; #pragma unroll
;     for (int i = 0; i < 16; ++i) v[i] = *(const f32x4*)(w.src + (size_t)i * w.N);
; __device__ __forceinline__ void nsa_unit(const Args& a, LAS unsigned char* lds, int b, int kvh, int qb) {
;     ...
; #pragma unroll 1
;     for (int it = 0; it <= nTot; ++it) {
;         if (it + 1 < nTot) asm volatile("s_waitcnt vmcnt(4) lgkmcnt(0)\n\ts_barrier" ::: "memory"); else asm volatile("s_waitcnt vmcnt(0) lgkmcnt(0)\n\ts_barrier" ::: "memory");
.Lcn_lgo_n0l:
	s_movk_i32 s12, 0x2000
	s_cmp_eq_u32 s1, 1
	s_cselect_b32 s12, 0x7000, s12
	v_and_b32_e32 v224, 63, v0
	v_and_b32_e32 v253, 7, v224
	v_lshrrev_b32_e32 v224, 3, v224
	v_lshlrev_b32_e32 v224, 2, v224
	v_lshlrev_b32_e32 v225, 4, v253
	v_lshlrev_b32_e32 v253, 2, v253
	v_mad_u32_u24 v254, v224, s12, v225
	global_load_dwordx4 v[212:215], v254, s[32:33] nt
	s_add_u32 s32, s32, s12
	s_addc_u32 s33, s33, 0
	global_load_dwordx4 v[216:219], v254, s[32:33] nt
	s_add_u32 s32, s32, s12
	s_addc_u32 s33, s33, 0
	global_load_dwordx4 v[220:223], v254, s[32:33] nt
	s_add_u32 s32, s32, s12
	s_addc_u32 s33, s33, 0
	global_load_dwordx2 v[224:225], v254, s[32:33] offset:0 nt
	global_load_dword v253, v254, s[32:33] offset:8 nt
	global_load_dword v254, v254, s[32:33] offset:12 nt
	s_add_i32 s74, s74, 1
	s_addk_i32 s75, 0x4000
	s_add_i32 s62, s62, 1
	s_cmp_eq_u32 s23, s74
	s_cbranch_scc1 .LBB0_919
.LBB0_897:
	s_cmp_ge_i32 s74, s15
	s_mov_b64 s[0:1], -1
	s_cbranch_scc0 .LBB0_900
	s_waitcnt vmcnt(10) lgkmcnt(0)
	s_barrier
	s_cbranch_execz .LBB0_901

; __device__ __forceinline__ void nsa_unit(const Args& a, LAS unsigned char* lds, int b, int kvh, int qb) {
;     ...
;         if (it + 1 < nTot) asm volatile("s_waitcnt vmcnt(4) lgkmcnt(0)\n\ts_barrier" ::: "memory"); else asm volatile("s_waitcnt vmcnt(0) lgkmcnt(0)\n\ts_barrier" ::: "memory");
.LBB0_901:
	s_waitcnt vmcnt(14) lgkmcnt(0)
	s_barrier
	s_cmp_lg_u32 s74, 0
	s_cselect_b64 s[0:1], -1, 0
	s_cmp_eq_u32 s74, 0
	s_cbranch_scc1 .LBB0_912

; __device__ __forceinline__ bf16x8 nsa_pack8(const f32x16& p, int s) { u32x4 w; w.x = pg8::cvt_pk_bf16(p[8 * s + 0], p[8 * s + 1]); w.y = pg8::cvt_pk_bf16(p[8 * s + 2], p[8 * s + 3]); w.z = pg8::cvt_pk_bf16(p[8 * s + 4], p[8 * s + 5]); w.w = pg8::cvt_pk_bf16(p[8 * s + 6], p[8 * s + 7]); return __builtin_bit_cast(bf16x8, w); }
; __device__ __forceinline__ void nsa_unit(const Args& a, LAS unsigned char* lds, int b, int kvh, int qb) {
;     ...
;             const float nmc = lane_on ? -mrun * SM_C : NINF;
;             float ls = 0.f;
; #pragma unroll
;             for (int i = 0; i < 16; ++i) { p0[i] = __builtin_amdgcn_exp2f(fmaf(p0[i], SM_C, nmc)); p1[i] = __builtin_amdgcn_exp2f(fmaf(p1[i], SM_C, nmc)); ls += p0[i] + p1[i]; }
;             lrun = lrun * alpha + ls;
;             pf[0][0] = nsa_pack8(p0, 0); pf[0][1] = nsa_pack8(p0, 1); pf[1][0] = nsa_pack8(p1, 0); pf[1][1] = nsa_pack8(p1, 1);
.LBB0_911:
	v_mul_f32_e32 v34, 0xbe0293ee, v208
	v_cndmask_b32_e64 v190, v244, v34, s[2:3]
	v_fmamk_f32 v34, v78, 0x3e0293ee, v190
	v_exp_f32_e32 v78, v34
	v_fmamk_f32 v34, v62, 0x3e0293ee, v190
	v_exp_f32_e32 v62, v34
	v_fmamk_f32 v34, v79, 0x3e0293ee, v190
	v_fmamk_f32 v36, v80, 0x3e0293ee, v190
	v_exp_f32_e32 v79, v34
	v_fmamk_f32 v34, v63, 0x3e0293ee, v190
	v_exp_f32_e32 v80, v36
	v_fmamk_f32 v36, v64, 0x3e0293ee, v190
	v_exp_f32_e32 v63, v34
	v_exp_f32_e32 v64, v36
	v_fmamk_f32 v36, v81, 0x3e0293ee, v190
	v_exp_f32_e32 v81, v36
	v_fmamk_f32 v36, v65, 0x3e0293ee, v190
	v_exp_f32_e32 v65, v36
	v_add_f32_e32 v34, v78, v62
	v_add_f32_e32 v34, 0, v34
	v_add_f32_e32 v35, v79, v63
	v_add_f32_e32 v34, v35, v34
	v_add_f32_e32 v35, v80, v64
	v_add_f32_e32 v34, v35, v34
	v_add_f32_e32 v35, v81, v65
	v_add_f32_e32 v50, v35, v34
	v_fmamk_f32 v34, v82, 0x3e0293ee, v190
	v_exp_f32_e32 v35, v34
	v_fmamk_f32 v34, v66, 0x3e0293ee, v190
	v_exp_f32_e32 v37, v34
	v_fmamk_f32 v34, v83, 0x3e0293ee, v190
	v_fmamk_f32 v36, v67, 0x3e0293ee, v190
	v_fmamk_f32 v38, v84, 0x3e0293ee, v190
	v_exp_f32_e32 v34, v34
	v_exp_f32_e32 v36, v36
	v_exp_f32_e32 v39, v38
	v_fmamk_f32 v38, v68, 0x3e0293ee, v190
	v_exp_f32_e32 v41, v38
	v_fmamk_f32 v38, v85, 0x3e0293ee, v190
	v_fmamk_f32 v40, v69, 0x3e0293ee, v190
	v_exp_f32_e32 v38, v38
	v_exp_f32_e32 v40, v40
	v_pk_add_f32 v[48:49], v[34:35], v[36:37]
	v_fmamk_f32 v52, v88, 0x3e0293ee, v190
	v_add_f32_e32 v49, v49, v50
	v_add_f32_e32 v50, v48, v49
	v_pk_add_f32 v[48:49], v[38:39], v[40:41]
	v_exp_f32_e32 v53, v52
	v_add_f32_e32 v49, v49, v50
	v_add_f32_e32 v58, v48, v49
	v_fmamk_f32 v48, v86, 0x3e0293ee, v190
	v_exp_f32_e32 v49, v48
	v_fmamk_f32 v48, v70, 0x3e0293ee, v190
	v_exp_f32_e32 v51, v48
	v_fmamk_f32 v48, v87, 0x3e0293ee, v190
	v_fmamk_f32 v50, v71, 0x3e0293ee, v190
	v_exp_f32_e32 v48, v48
	v_exp_f32_e32 v50, v50
	v_fmamk_f32 v52, v72, 0x3e0293ee, v190
	v_exp_f32_e32 v55, v52
	v_fmamk_f32 v52, v89, 0x3e0293ee, v190
	v_fmamk_f32 v54, v73, 0x3e0293ee, v190
	v_exp_f32_e32 v52, v52
	v_exp_f32_e32 v54, v54
	v_pk_add_f32 v[56:57], v[48:49], v[50:51]
	v_fmamk_f32 v60, v92, 0x3e0293ee, v190
	v_add_f32_e32 v57, v57, v58
	v_add_f32_e32 v58, v56, v57
	v_pk_add_f32 v[56:57], v[52:53], v[54:55]
	v_exp_f32_e32 v61, v60
	v_add_f32_e32 v57, v57, v58
	v_add_f32_e32 v68, v56, v57
	v_fmamk_f32 v56, v90, 0x3e0293ee, v190
	v_exp_f32_e32 v57, v56
	v_fmamk_f32 v56, v74, 0x3e0293ee, v190
	v_exp_f32_e32 v59, v56
	v_fmamk_f32 v56, v91, 0x3e0293ee, v190
	v_fmamk_f32 v58, v75, 0x3e0293ee, v190
	v_exp_f32_e32 v56, v56
	v_exp_f32_e32 v58, v58
	v_fmamk_f32 v60, v76, 0x3e0293ee, v190
	v_exp_f32_e32 v211, v60
	v_fmamk_f32 v60, v93, 0x3e0293ee, v190
	v_fmac_f32_e32 v190, 0x3e0293ee, v77
	v_exp_f32_e32 v60, v60
	v_exp_f32_e32 v210, v190
	v_pk_add_f32 v[66:67], v[56:57], v[58:59]
	v_add_f32_e32 v67, v67, v68
	v_add_f32_e32 v66, v66, v67
	v_pk_add_f32 v[190:191], v[60:61], v[210:211]
	v_add_f32_e32 v191, v191, v66
	v_add_f32_e32 v192, v190, v191
	v_fmac_f32_e32 v192, v209, v46
	v_mov_b32_e32 v209, v192
	v_cvt_pk_bf16_f32 v190, v78, v79
	v_cvt_pk_bf16_f32 v191, v80, v81
	v_cvt_pk_bf16_f32 v192, v35, v34
	v_cvt_pk_bf16_f32 v193, v39, v38
	v_cvt_pk_bf16_f32 v194, v49, v48
	v_cvt_pk_bf16_f32 v195, v53, v52
	v_cvt_pk_bf16_f32 v196, v57, v56
	v_cvt_pk_bf16_f32 v197, v61, v60
	v_cvt_pk_bf16_f32 v198, v62, v63
	v_cvt_pk_bf16_f32 v199, v64, v65
	v_cvt_pk_bf16_f32 v200, v37, v36
	v_cvt_pk_bf16_f32 v201, v41, v40
	v_cvt_pk_bf16_f32 v202, v51, v50
	v_cvt_pk_bf16_f32 v203, v55, v54
	v_cvt_pk_bf16_f32 v204, v59, v58
	v_cvt_pk_bf16_f32 v205, v211, v210

; #define GAS __attribute__((address_space(1)))
; #define LAS __attribute__((address_space(3)))
; __device__ __forceinline__ unsigned cvt_pk_bf16(float lo, float hi) { unsigned r; asm volatile("v_cvt_pk_bf16_f32 %0, %1, %2" : "=v"(r) : "v"(lo), "v"(hi)); return r; }
; __device__ __forceinline__ void nsa_pv_rd4(const LAS unsigned char* vA, int sv, int step, bf16x8 (&af)[4]) {
; #pragma unroll
;     for (int dt = 0; dt < 4; ++dt) af[dt] = *(const LAS bf16x8*)(vA + dt * 4096 + (((2 * step) * 16) ^ sv));
; }
; __device__ __forceinline__ void nsa_pv_mm4(const bf16x8 (&af)[4], const bf16x8& pfk, f32x16 (&o)[4]) {
; #pragma unroll
;     for (int dt = 0; dt < 4; ++dt) o[dt] = __builtin_amdgcn_mfma_f32_32x32x16_bf16(af[dt], pfk, o[dt], 0, 0, 0);
; }
; __device__ __forceinline__ void nsa_pv_sw(const LAS unsigned char* vbuf, const bf16x8 (&pf)[2][2], f32x16 (&o)[4], int r, int h) {
;     const int sv = (((r >> 1) & 7) ^ h) * 16; const LAS unsigned char* vA = vbuf + r * 128;
; #pragma unroll
;     for (int step = 0; step < 4; ++step) { bf16x8 fa[4];
;         nsa_pv_rd4(vA, sv, step, fa); __builtin_amdgcn_sched_barrier(0);
;         nsa_pv_mm4(fa, pf[step >> 1][step & 1], o); __builtin_amdgcn_sched_barrier(0); }
; __device__ __forceinline__ void nsa_unit(const Args& a, LAS unsigned char* lds, int b, int kvh, int qb) {
;     ...
;             nsa_pv_sw(lds + VOFF + (ti & 3) * NTB, pf, o, ro, ho);
;             if (ti == nS - 1 || ti == nTot - 1) {
;                 const float lt = lrun + __shfl_xor(lrun, 32); const float f = ((ti == nS - 1) ? g1 : g2) / lt;
; #pragma unroll
;                 for (int dt = 0; dt < 4; ++dt) {
; #pragma unroll
;                     for (int aa = 0; aa < 4; ++aa) { const u32x2 pv = *(const GAS u32x2*)(mp + (32 * dt + 8 * aa) * 2); u32x2 wv;
;                         wv.x = pg8::cvt_pk_bf16(bflo(pv.x) + o[dt][4 * aa] * f, bfhi(pv.x) + o[dt][4 * aa + 1] * f); wv.y = pg8::cvt_pk_bf16(bflo(pv.y) + o[dt][4 * aa + 2] * f, bfhi(pv.y) + o[dt][4 * aa + 3] * f);
;                         *(GAS u32x2*)(mp + (32 * dt + 8 * aa) * 2) = wv; }
.LBB0_914:
	v_mov_b32_e32 v211, v233
	v_mov_b32_e32 v210, v232
	s_andn2_b64 vcc, exec, s[0:1]
	s_cbranch_vccnz .LBB0_917
	s_and_b32 s0, s75, 0xc000
	v_lshrrev_b32_e32 v34, 1, v210
	s_add_i32 s0, s0, 0
	v_bitop3_b32 v34, v34, v211, 7 bitop3:0x6c
	v_lshlrev_b32_e32 v46, 4, v34
	v_lshl_add_u32 v56, v210, 7, s0
	v_add_u32_e32 v52, v56, v46
	ds_read_b128 v[34:37], v52 offset:49152
	ds_read_b128 v[38:41], v52 offset:53248
	ds_read_b128 v[48:51], v52 offset:57344
	ds_read_b128 v[52:55], v52 offset:61440
	s_waitcnt lgkmcnt(3)
	v_mfma_f32_32x32x16_bf16 v[142:157], v[34:37], v[190:193], v[142:157]
	s_waitcnt lgkmcnt(2)
	v_mfma_f32_32x32x16_bf16 v[126:141], v[38:41], v[190:193], v[126:141]
	s_waitcnt lgkmcnt(1)
	v_mfma_f32_32x32x16_bf16 v[110:125], v[48:51], v[190:193], v[110:125]
	s_waitcnt lgkmcnt(0)
	v_mfma_f32_32x32x16_bf16 v[94:109], v[52:55], v[190:193], v[94:109]
	v_xad_u32 v52, v46, 32, v56
	ds_read_b128 v[34:37], v52 offset:49152
	ds_read_b128 v[38:41], v52 offset:53248
	ds_read_b128 v[48:51], v52 offset:57344
	ds_read_b128 v[52:55], v52 offset:61440
	s_waitcnt lgkmcnt(3)
	v_mfma_f32_32x32x16_bf16 v[142:157], v[34:37], v[194:197], v[142:157]
	s_waitcnt lgkmcnt(2)
	v_mfma_f32_32x32x16_bf16 v[126:141], v[38:41], v[194:197], v[126:141]
	s_waitcnt lgkmcnt(1)
	v_mfma_f32_32x32x16_bf16 v[110:125], v[48:51], v[194:197], v[110:125]
	s_waitcnt lgkmcnt(0)
	v_mfma_f32_32x32x16_bf16 v[94:109], v[52:55], v[194:197], v[94:109]
	v_xad_u32 v52, v46, 64, v56
	ds_read_b128 v[34:37], v52 offset:49152
	ds_read_b128 v[38:41], v52 offset:53248
	ds_read_b128 v[48:51], v52 offset:57344
	ds_read_b128 v[52:55], v52 offset:61440
	s_waitcnt lgkmcnt(3)
	v_mfma_f32_32x32x16_bf16 v[142:157], v[34:37], v[198:201], v[142:157]
	s_waitcnt lgkmcnt(2)
	v_mfma_f32_32x32x16_bf16 v[126:141], v[38:41], v[198:201], v[126:141]
	s_waitcnt lgkmcnt(1)
	v_mfma_f32_32x32x16_bf16 v[110:125], v[48:51], v[198:201], v[110:125]
	s_waitcnt lgkmcnt(0)
	v_mfma_f32_32x32x16_bf16 v[94:109], v[52:55], v[198:201], v[94:109]
	v_xad_u32 v46, v46, s68, v56
	ds_read_b128 v[34:37], v46 offset:49152
	ds_read_b128 v[38:41], v46 offset:53248
	ds_read_b128 v[48:51], v46 offset:57344
	ds_read_b128 v[52:55], v46 offset:61440
	s_waitcnt lgkmcnt(3)
	v_mfma_f32_32x32x16_bf16 v[142:157], v[34:37], v[202:205], v[142:157]
	s_waitcnt lgkmcnt(2)
	v_mfma_f32_32x32x16_bf16 v[126:141], v[38:41], v[202:205], v[126:141]
	s_waitcnt lgkmcnt(1)
	v_mfma_f32_32x32x16_bf16 v[110:125], v[48:51], v[202:205], v[110:125]
	s_waitcnt lgkmcnt(0)
	v_mfma_f32_32x32x16_bf16 v[94:109], v[52:55], v[202:205], v[94:109]
	s_cmp_eq_u32 s14, s74
	s_cselect_b64 s[12:13], -1, 0
	s_cmp_eq_u32 s24, s74
	s_cselect_b64 s[0:1], -1, 0
	s_or_b64 s[0:1], s[12:13], s[0:1]
	s_andn2_b64 vcc, exec, s[0:1]
	s_cbranch_vccnz .LBB0_917
	ds_bpermute_b32 v229, v252, v209
	v_cndmask_b32_e64 v208, v251, v250, s[12:13]
	v_mov_b32_e32 v60, v47
	v_mov_b32_e32 v61, v47
	v_mov_b32_e32 v48, v47
	s_waitcnt lgkmcnt(0)
	v_pk_add_f32 v[34:35], v[208:209], v[228:229]
	v_mov_b32_e32 v49, v47
	v_div_scale_f32 v36, s[0:1], v34, v34, 1.0
	v_rcp_f32_e32 v37, v36
	v_mov_b32_e32 v50, v47
	v_mov_b32_e32 v51, v47
	v_mov_b32_e32 v52, v47
	v_fma_f32 v38, -v36, v37, 1.0
	v_fmac_f32_e32 v37, v38, v37
	v_div_scale_f32 v38, vcc, 1.0, v34, 1.0
	v_mul_f32_e32 v39, v38, v37
	v_fma_f32 v40, -v36, v39, v38
	v_fmac_f32_e32 v39, v40, v37
	v_fma_f32 v36, -v36, v39, v38
	v_div_fmas_f32 v36, v36, v37, v39
	v_div_fixup_f32 v34, v36, v34, 1.0
	v_div_scale_f32 v36, s[0:1], v35, v35, v34
	v_rcp_f32_e32 v37, v36
	v_mov_b32_e32 v53, v47
	v_mov_b32_e32 v54, v47
	v_mov_b32_e32 v55, v47
	v_fma_f32 v38, -v36, v37, 1.0
	v_fmac_f32_e32 v37, v38, v37
	v_div_scale_f32 v38, vcc, v34, v35, v34
	v_mul_f32_e32 v39, v38, v37
	v_fma_f32 v40, -v36, v39, v38
	v_fmac_f32_e32 v39, v40, v37
	v_fma_f32 v36, -v36, v39, v38
	v_div_fmas_f32 v36, v36, v37, v39
	v_div_fixup_f32 v46, v36, v35, v34
	v_mov_b32_e32 v56, v47
	v_mov_b32_e32 v57, v47
	v_mov_b32_e32 v58, v47
	v_mov_b32_e32 v59, v47
	v_mov_b32_e32 v208, 0xf149f2ca
	v_mov_b32_e32 v209, 0
	global_load_dwordx2 v[62:63], v[206:207], off
	global_load_dwordx2 v[64:65], v[206:207], off offset:16
	global_load_dwordx2 v[66:67], v[206:207], off offset:32
	global_load_dwordx2 v[68:69], v[206:207], off offset:48
	global_load_dwordx2 v[70:71], v[206:207], off offset:64
	global_load_dwordx2 v[72:73], v[206:207], off offset:80
	global_load_dwordx2 v[74:75], v[206:207], off offset:96
	global_load_dwordx2 v[76:77], v[206:207], off offset:112
	global_load_dwordx2 v[78:79], v[206:207], off offset:128
	global_load_dwordx2 v[80:81], v[206:207], off offset:144
	global_load_dwordx2 v[82:83], v[206:207], off offset:160
	global_load_dwordx2 v[84:85], v[206:207], off offset:176
	global_load_dwordx2 v[86:87], v[206:207], off offset:192
	global_load_dwordx2 v[88:89], v[206:207], off offset:208
	global_load_dwordx2 v[90:91], v[206:207], off offset:224
	global_load_dwordx2 v[92:93], v[206:207], off offset:240
	s_waitcnt vmcnt(15)
	v_lshlrev_b32_e32 v36, 16, v62
	v_and_b32_e32 v34, 0xffff0000, v62
	v_fmac_f32_e32 v36, v142, v46
	v_fmac_f32_e32 v34, v143, v46
	v_cvt_pk_bf16_f32 v34, v36, v34
	v_lshlrev_b32_e32 v36, 16, v63
	v_and_b32_e32 v35, 0xffff0000, v63
	v_fmac_f32_e32 v35, v145, v46
	v_fmac_f32_e32 v36, v144, v46
	v_cvt_pk_bf16_f32 v35, v36, v35
	global_store_dwordx2 v[206:207], v[34:35], off
	s_waitcnt vmcnt(15)
	v_lshlrev_b32_e32 v36, 16, v64
	v_and_b32_e32 v34, 0xffff0000, v64
	v_fmac_f32_e32 v36, v146, v46
	v_fmac_f32_e32 v34, v147, v46
	v_cvt_pk_bf16_f32 v34, v36, v34
	v_lshlrev_b32_e32 v36, 16, v65
	v_and_b32_e32 v35, 0xffff0000, v65
	v_fmac_f32_e32 v35, v149, v46
	v_fmac_f32_e32 v36, v148, v46
	v_cvt_pk_bf16_f32 v35, v36, v35
	global_store_dwordx2 v[206:207], v[34:35], off offset:16
	s_waitcnt vmcnt(15)
; #define GAS __attribute__((address_space(1)))
; __device__ __forceinline__ unsigned cvt_pk_bf16(float lo, float hi) { unsigned r; asm volatile("v_cvt_pk_bf16_f32 %0, %1, %2" : "=v"(r) : "v"(lo), "v"(hi)); return r; }
; __device__ __forceinline__ void nsa_unit(const Args& a, LAS unsigned char* lds, int b, int kvh, int qb) {
;     ...
;                     for (int aa = 0; aa < 4; ++aa) { const u32x2 pv = *(const GAS u32x2*)(mp + (32 * dt + 8 * aa) * 2); u32x2 wv;
;                         wv.x = pg8::cvt_pk_bf16(bflo(pv.x) + o[dt][4 * aa] * f, bfhi(pv.x) + o[dt][4 * aa + 1] * f); wv.y = pg8::cvt_pk_bf16(bflo(pv.y) + o[dt][4 * aa + 2] * f, bfhi(pv.y) + o[dt][4 * aa + 3] * f);
;                         *(GAS u32x2*)(mp + (32 * dt + 8 * aa) * 2) = wv; }
; #pragma unroll
;                     for (int i = 0; i < 16; ++i) o[dt][i] = 0.f; }
;                 mrun = -1e30f; lrun = 0.f;
;                 asm volatile("s_waitcnt vmcnt(0)" ::: "memory");
	v_lshlrev_b32_e32 v36, 16, v66
	v_and_b32_e32 v34, 0xffff0000, v66
	v_fmac_f32_e32 v36, v150, v46
	v_fmac_f32_e32 v34, v151, v46
	v_cvt_pk_bf16_f32 v34, v36, v34
	v_lshlrev_b32_e32 v36, 16, v67
	v_and_b32_e32 v35, 0xffff0000, v67
	v_fmac_f32_e32 v35, v153, v46
	v_fmac_f32_e32 v36, v152, v46
	v_cvt_pk_bf16_f32 v35, v36, v35
	global_store_dwordx2 v[206:207], v[34:35], off offset:32
	s_waitcnt vmcnt(15)
	v_lshlrev_b32_e32 v36, 16, v68
	v_and_b32_e32 v34, 0xffff0000, v68
	v_fmac_f32_e32 v36, v154, v46
	v_fmac_f32_e32 v34, v155, v46
	v_cvt_pk_bf16_f32 v34, v36, v34
	v_lshlrev_b32_e32 v36, 16, v69
	v_and_b32_e32 v35, 0xffff0000, v69
	v_fmac_f32_e32 v35, v157, v46
	v_fmac_f32_e32 v36, v156, v46
	v_cvt_pk_bf16_f32 v35, v36, v35
	global_store_dwordx2 v[206:207], v[34:35], off offset:48
	s_waitcnt vmcnt(15)
	v_lshlrev_b32_e32 v36, 16, v70
	v_and_b32_e32 v34, 0xffff0000, v70
	v_fmac_f32_e32 v36, v126, v46
	v_fmac_f32_e32 v34, v127, v46
	v_cvt_pk_bf16_f32 v34, v36, v34
	v_lshlrev_b32_e32 v36, 16, v71
	v_and_b32_e32 v35, 0xffff0000, v71
	v_fmac_f32_e32 v35, v129, v46
	v_fmac_f32_e32 v36, v128, v46
	v_cvt_pk_bf16_f32 v35, v36, v35
	global_store_dwordx2 v[206:207], v[34:35], off offset:64
	s_waitcnt vmcnt(15)
	v_lshlrev_b32_e32 v36, 16, v72
	v_and_b32_e32 v34, 0xffff0000, v72
	v_fmac_f32_e32 v36, v130, v46
	v_fmac_f32_e32 v34, v131, v46
	v_cvt_pk_bf16_f32 v34, v36, v34
	v_lshlrev_b32_e32 v36, 16, v73
	v_and_b32_e32 v35, 0xffff0000, v73
	v_fmac_f32_e32 v35, v133, v46
	v_fmac_f32_e32 v36, v132, v46
	v_cvt_pk_bf16_f32 v35, v36, v35
	global_store_dwordx2 v[206:207], v[34:35], off offset:80
	s_waitcnt vmcnt(15)
	v_lshlrev_b32_e32 v36, 16, v74
	v_and_b32_e32 v34, 0xffff0000, v74
	v_fmac_f32_e32 v36, v134, v46
	v_fmac_f32_e32 v34, v135, v46
	v_cvt_pk_bf16_f32 v34, v36, v34
	v_lshlrev_b32_e32 v36, 16, v75
	v_and_b32_e32 v35, 0xffff0000, v75
	v_fmac_f32_e32 v35, v137, v46
	v_fmac_f32_e32 v36, v136, v46
	v_cvt_pk_bf16_f32 v35, v36, v35
	global_store_dwordx2 v[206:207], v[34:35], off offset:96
	s_waitcnt vmcnt(15)
	v_lshlrev_b32_e32 v36, 16, v76
	v_and_b32_e32 v34, 0xffff0000, v76
	v_fmac_f32_e32 v36, v138, v46
	v_fmac_f32_e32 v34, v139, v46
	v_cvt_pk_bf16_f32 v34, v36, v34
	v_lshlrev_b32_e32 v36, 16, v77
	v_and_b32_e32 v35, 0xffff0000, v77
	v_fmac_f32_e32 v35, v141, v46
	v_fmac_f32_e32 v36, v140, v46
	v_cvt_pk_bf16_f32 v35, v36, v35
	global_store_dwordx2 v[206:207], v[34:35], off offset:112
	s_waitcnt vmcnt(15)
	v_lshlrev_b32_e32 v36, 16, v78
	v_and_b32_e32 v34, 0xffff0000, v78
	v_fmac_f32_e32 v36, v110, v46
	v_fmac_f32_e32 v34, v111, v46
	v_cvt_pk_bf16_f32 v34, v36, v34
	v_lshlrev_b32_e32 v36, 16, v79
	v_and_b32_e32 v35, 0xffff0000, v79
	v_fmac_f32_e32 v35, v113, v46
	v_fmac_f32_e32 v36, v112, v46
	v_cvt_pk_bf16_f32 v35, v36, v35
	global_store_dwordx2 v[206:207], v[34:35], off offset:128
	s_waitcnt vmcnt(15)
	v_lshlrev_b32_e32 v36, 16, v80
	v_and_b32_e32 v34, 0xffff0000, v80
	v_fmac_f32_e32 v36, v114, v46
	v_fmac_f32_e32 v34, v115, v46
	v_cvt_pk_bf16_f32 v34, v36, v34
	v_lshlrev_b32_e32 v36, 16, v81
	v_and_b32_e32 v35, 0xffff0000, v81
	v_fmac_f32_e32 v35, v117, v46
	v_fmac_f32_e32 v36, v116, v46
	v_cvt_pk_bf16_f32 v35, v36, v35
	global_store_dwordx2 v[206:207], v[34:35], off offset:144
	s_waitcnt vmcnt(15)
	v_lshlrev_b32_e32 v36, 16, v82
	v_and_b32_e32 v34, 0xffff0000, v82
	v_fmac_f32_e32 v36, v118, v46
	v_fmac_f32_e32 v34, v119, v46
	v_cvt_pk_bf16_f32 v34, v36, v34
	v_lshlrev_b32_e32 v36, 16, v83
	v_and_b32_e32 v35, 0xffff0000, v83
	v_fmac_f32_e32 v35, v121, v46
	v_fmac_f32_e32 v36, v120, v46
	v_cvt_pk_bf16_f32 v35, v36, v35
	global_store_dwordx2 v[206:207], v[34:35], off offset:160
	s_waitcnt vmcnt(15)
	v_lshlrev_b32_e32 v36, 16, v84
	v_and_b32_e32 v34, 0xffff0000, v84
	v_fmac_f32_e32 v36, v122, v46
	v_fmac_f32_e32 v34, v123, v46
	v_cvt_pk_bf16_f32 v34, v36, v34
	v_lshlrev_b32_e32 v36, 16, v85
	v_and_b32_e32 v35, 0xffff0000, v85
	v_fmac_f32_e32 v35, v125, v46
	v_fmac_f32_e32 v36, v124, v46
	v_cvt_pk_bf16_f32 v35, v36, v35
	global_store_dwordx2 v[206:207], v[34:35], off offset:176
	s_waitcnt vmcnt(15)
	v_lshlrev_b32_e32 v36, 16, v86
	v_and_b32_e32 v34, 0xffff0000, v86
	v_fmac_f32_e32 v36, v94, v46
	v_fmac_f32_e32 v34, v95, v46
	v_cvt_pk_bf16_f32 v34, v36, v34
	v_lshlrev_b32_e32 v36, 16, v87
	v_and_b32_e32 v35, 0xffff0000, v87
	v_fmac_f32_e32 v35, v97, v46
	v_fmac_f32_e32 v36, v96, v46
	v_cvt_pk_bf16_f32 v35, v36, v35
	global_store_dwordx2 v[206:207], v[34:35], off offset:192
	s_waitcnt vmcnt(15)
	v_lshlrev_b32_e32 v36, 16, v88
	v_and_b32_e32 v34, 0xffff0000, v88
	v_fmac_f32_e32 v36, v98, v46
	v_fmac_f32_e32 v34, v99, v46
	v_cvt_pk_bf16_f32 v34, v36, v34
	v_lshlrev_b32_e32 v36, 16, v89
	v_and_b32_e32 v35, 0xffff0000, v89
	v_fmac_f32_e32 v35, v101, v46
	v_fmac_f32_e32 v36, v100, v46
	v_cvt_pk_bf16_f32 v35, v36, v35
	global_store_dwordx2 v[206:207], v[34:35], off offset:208
	s_waitcnt vmcnt(15)
	v_lshlrev_b32_e32 v36, 16, v90
	v_and_b32_e32 v34, 0xffff0000, v90
	v_fmac_f32_e32 v36, v102, v46
	v_fmac_f32_e32 v34, v103, v46
	v_cvt_pk_bf16_f32 v34, v36, v34
	v_lshlrev_b32_e32 v36, 16, v91
	v_and_b32_e32 v35, 0xffff0000, v91
	v_fmac_f32_e32 v35, v105, v46
	v_fmac_f32_e32 v36, v104, v46
	v_cvt_pk_bf16_f32 v35, v36, v35
	global_store_dwordx2 v[206:207], v[34:35], off offset:224
	s_waitcnt vmcnt(15)
	v_lshlrev_b32_e32 v36, 16, v92
	v_and_b32_e32 v34, 0xffff0000, v92
	v_fmac_f32_e32 v36, v106, v46
	v_fmac_f32_e32 v34, v107, v46
	v_cvt_pk_bf16_f32 v34, v36, v34
	v_lshlrev_b32_e32 v36, 16, v93
	v_and_b32_e32 v35, 0xffff0000, v93
	v_fmac_f32_e32 v35, v109, v46
	v_fmac_f32_e32 v36, v108, v46
	v_cvt_pk_bf16_f32 v35, v36, v35
	global_store_dwordx2 v[206:207], v[34:35], off offset:240
	s_waitcnt vmcnt(0)
	v_mov_b32_e32 v46, v47
	v_mov_b64_e32 v[156:157], v[60:61]
	v_mov_b64_e32 v[140:141], v[60:61]
	v_mov_b64_e32 v[124:125], v[60:61]
	v_mov_b64_e32 v[108:109], v[60:61]
	v_mov_b64_e32 v[154:155], v[58:59]
	v_mov_b64_e32 v[152:153], v[56:57]
	v_mov_b64_e32 v[150:151], v[54:55]
	v_mov_b64_e32 v[148:149], v[52:53]
	v_mov_b64_e32 v[146:147], v[50:51]
	v_mov_b64_e32 v[144:145], v[48:49]
	v_mov_b64_e32 v[142:143], v[46:47]
	v_mov_b64_e32 v[138:139], v[58:59]
	v_mov_b64_e32 v[136:137], v[56:57]
	v_mov_b64_e32 v[134:135], v[54:55]
	v_mov_b64_e32 v[132:133], v[52:53]
	v_mov_b64_e32 v[130:131], v[50:51]
	v_mov_b64_e32 v[128:129], v[48:49]
	v_mov_b64_e32 v[126:127], v[46:47]
	v_mov_b64_e32 v[122:123], v[58:59]
	v_mov_b64_e32 v[120:121], v[56:57]
	v_mov_b64_e32 v[118:119], v[54:55]
	v_mov_b64_e32 v[116:117], v[52:53]
	v_mov_b64_e32 v[114:115], v[50:51]
	v_mov_b64_e32 v[112:113], v[48:49]
	v_mov_b64_e32 v[110:111], v[46:47]
	v_mov_b64_e32 v[106:107], v[58:59]
	v_mov_b64_e32 v[104:105], v[56:57]
	v_mov_b64_e32 v[102:103], v[54:55]
	v_mov_b64_e32 v[100:101], v[52:53]
	v_mov_b64_e32 v[98:99], v[50:51]
	v_mov_b64_e32 v[96:97], v[48:49]
	v_mov_b64_e32 v[94:95], v[46:47]
; #define LAS __attribute__((address_space(3)))
; __device__ __forceinline__ void nsa_qk_sw(const LAS unsigned char* kbuf, const bf16x8 (&qf)[8], int r, int h, f32x16& p0, f32x16& p1) {
;     const int x = r & 15; const LAS unsigned char* kA = kbuf + r * 256 + ((h ^ (x & 1)) * 16); const int xk = (x & 14) * 16;
; #pragma unroll
;     for (int i = 0; i < 16; ++i) { p0[i] = 0.f; p1[i] = 0.f; }
;     bf16x8 a0, a1, b0, b1;
;     a0 = *(const LAS bf16x8*)(kA + (0 ^ xk)); a1 = *(const LAS bf16x8*)(kA + (0 ^ xk) + 8192); __builtin_amdgcn_sched_barrier(0);
; #pragma unroll
;     for (int ks = 0; ks < 8; ks += 2) {
;         b0 = *(const LAS bf16x8*)(kA + (((ks + 1) * 32) ^ xk)); b1 = *(const LAS bf16x8*)(kA + (((ks + 1) * 32) ^ xk) + 8192); __builtin_amdgcn_sched_barrier(0);
;         p0 = __builtin_amdgcn_mfma_f32_32x32x16_bf16(a0, qf[ks], p0, 0, 0, 0); p1 = __builtin_amdgcn_mfma_f32_32x32x16_bf16(a1, qf[ks], p1, 0, 0, 0); __builtin_amdgcn_sched_barrier(0);
;         if (ks + 2 < 8) { a0 = *(const LAS bf16x8*)(kA + (((ks + 2) * 32) ^ xk)); a1 = *(const LAS bf16x8*)(kA + (((ks + 2) * 32) ^ xk) + 8192); } __builtin_amdgcn_sched_barrier(0);
;         p0 = __builtin_amdgcn_mfma_f32_32x32x16_bf16(b0, qf[ks + 1], p0, 0, 0, 0); p1 = __builtin_amdgcn_mfma_f32_32x32x16_bf16(b1, qf[ks + 1], p1, 0, 0, 0); __builtin_amdgcn_sched_barrier(0);
;     }
; __device__ __forceinline__ void nsa_unit(const Args& a, LAS unsigned char* lds, int b, int kvh, int qb) {
;     ...
;         if (it < nTot) nsa_qk_sw(lds + (it % 3) * NTB, qf, ro, ho, p0, p1);
.LBB0_917:
	s_cmp_gt_i32 s74, s15
	s_cbranch_scc1 .LBB0_896
	s_mul_hi_u32 s0, s74, 0xaaaaaaab
	s_lshr_b32 s0, s0, 1
	v_lshlrev_b32_e32 v57, 4, v210
	s_mul_i32 s0, s0, 0xffff4000
	v_lshlrev_b32_e32 v46, 8, v210
	v_bitop3_b32 v34, v210, v211, 1 bitop3:0x6c
	v_and_b32_e32 v58, 0xe0, v57
	s_add_i32 s1, s75, 0
	v_lshlrev_b32_e32 v56, 4, v34
	v_or_b32_e32 v34, v46, v58
	s_add_i32 s1, s1, s0
	v_add3_u32 v38, v34, v56, s1
	ds_read_b128 v[34:37], v38 offset:16384
	ds_read_b128 v[38:41], v38 offset:24576
	v_bitop3_b32 v48, v58, v46, 32 bitop3:0xde
	v_add3_u32 v52, v48, v56, s1
	ds_read_b128 v[48:51], v52 offset:16384
	ds_read_b128 v[52:55], v52 offset:24576
	s_waitcnt lgkmcnt(3)
	v_mfma_f32_32x32x16_bf16 v[78:93], v[34:37], v[182:185], 0
	s_waitcnt lgkmcnt(2)
	v_mfma_f32_32x32x16_bf16 v[62:77], v[38:41], v[182:185], 0
	v_bitop3_b32 v34, v58, v46, 64 bitop3:0xde
	v_add3_u32 v38, v34, v56, s1
	ds_read_b128 v[34:37], v38 offset:24576
	ds_read_b128 v[38:41], v38 offset:16384
	s_waitcnt lgkmcnt(3)
	v_mfma_f32_32x32x16_bf16 v[78:93], v[48:51], v[186:189], v[78:93]
	s_waitcnt lgkmcnt(2)
	v_mfma_f32_32x32x16_bf16 v[62:77], v[52:55], v[186:189], v[62:77]
	v_bitop3_b32 v48, v58, v46, s68 bitop3:0xde
	v_add3_u32 v52, v48, v56, s1
	ds_read_b128 v[48:51], v52 offset:16384
	ds_read_b128 v[52:55], v52 offset:24576
	s_waitcnt lgkmcnt(2)
	v_mfma_f32_32x32x16_bf16 v[78:93], v[38:41], v[158:161], v[78:93]
	v_mfma_f32_32x32x16_bf16 v[62:77], v[34:37], v[158:161], v[62:77]
	s_movk_i32 s0, 0x80
	v_bitop3_b32 v34, v58, v46, s0 bitop3:0xde
	v_add3_u32 v38, v34, v56, s1
	ds_read_b128 v[34:37], v38 offset:24576
	ds_read_b128 v[38:41], v38 offset:16384
	s_waitcnt lgkmcnt(3)
	v_mfma_f32_32x32x16_bf16 v[78:93], v[48:51], v[162:165], v[78:93]
	s_waitcnt lgkmcnt(2)
	v_mfma_f32_32x32x16_bf16 v[62:77], v[52:55], v[162:165], v[62:77]
	s_movk_i32 s0, 0xa0
	v_bitop3_b32 v48, v58, v46, s0 bitop3:0xde
	v_add3_u32 v52, v48, v56, s1
	ds_read_b128 v[48:51], v52 offset:16384
	ds_read_b128 v[52:55], v52 offset:24576
	s_waitcnt lgkmcnt(2)
	v_mfma_f32_32x32x16_bf16 v[78:93], v[38:41], v[166:169], v[78:93]
	v_mfma_f32_32x32x16_bf16 v[62:77], v[34:37], v[166:169], v[62:77]
	s_movk_i32 s0, 0xc0
	v_bitop3_b32 v34, v58, v46, s0 bitop3:0xde
	v_add3_u32 v38, v34, v56, s1
	ds_read_b128 v[34:37], v38 offset:24576
	ds_read_b128 v[38:41], v38 offset:16384
	s_waitcnt lgkmcnt(3)
	v_mfma_f32_32x32x16_bf16 v[78:93], v[48:51], v[170:173], v[78:93]
	s_waitcnt lgkmcnt(2)
	v_mfma_f32_32x32x16_bf16 v[62:77], v[52:55], v[170:173], v[62:77]
	s_movk_i32 s0, 0xe0
	v_bitop3_b32 v46, v57, v46, s0 bitop3:0xce
	v_add3_u32 v46, v46, v56, s1
	ds_read_b128 v[48:51], v46 offset:16384
	ds_read_b128 v[52:55], v46 offset:24576
	s_waitcnt lgkmcnt(2)
	v_mfma_f32_32x32x16_bf16 v[78:93], v[38:41], v[174:177], v[78:93]
	v_mfma_f32_32x32x16_bf16 v[62:77], v[34:37], v[174:177], v[62:77]
	s_waitcnt lgkmcnt(1)
	v_mfma_f32_32x32x16_bf16 v[78:93], v[48:51], v[178:181], v[78:93]
	s_waitcnt lgkmcnt(0)
	v_mfma_f32_32x32x16_bf16 v[62:77], v[52:55], v[178:181], v[62:77]
	s_branch .LBB0_896
.LBB0_919:
	s_waitcnt vmcnt(0)
	s_bitcmp1_b32 s101, 31
	s_cbranch_scc0 .Lcn_snone_n0x
	s_and_b32 s12, s101, 0x7fffffff
	s_sub_u32 s12, s12, 1
	s_mul_i32 s13, s12, 0x2493
	s_lshr_b32 s13, s13, 16
	s_mul_i32 s65, s13, 7
	s_sub_u32 s65, s12, s65
	s_lshl_b32 s65, s65, 11
	s_add_u32 s65, s65, s100
	s_cmp_ge_u32 s13, 16
	s_cbranch_scc1 .Lcn_dn_n0xd
	s_lshr_b32 s66, s65, 5
	s_mul_i32 s66, s66, 0x2493
	s_lshr_b32 s66, s66, 16
	s_mul_i32 s67, s66, 0xe0
	s_sub_u32 s67, s65, s67
	s_and_b32 s65, s13, 1
	s_lshr_b32 s13, s13, 1
	s_mul_i32 s12, s13, 0x1c00000
	s_add_u32 s12, s12, 0x4a000000
	s_lshr_b32 s13, s67, 2
	s_lshl_b32 s13, s13, 8
	s_lshl_b32 s65, s65, 7
	s_add_u32 s13, s13, s65
	s_and_b32 s65, s67, 3
	s_lshl_b32 s65, s65, 5
	s_add_u32 s13, s13, s65
	s_lshl_b32 s13, s13, 11
	s_add_u32 s12, s12, s13
	s_lshl_b32 s13, s66, 5
	s_add_u32 s12, s12, s13
	v_readlane_b32 s32, v255, 52
	v_readlane_b32 s33, v255, 53
	s_add_u32 s32, s32, s12
	s_addc_u32 s33, s33, 0
	s_mov_b32 s1, 1
	s_branch .Lcn_dd_n0xd

; __device__ __forceinline__ void p0_weights(const Args& a, LAS unsigned char* lds) {
;     ...
;         else if ((r -= I_FD) < 16 * I_MG) { const int up = r / (8 * I_MG); r -= up * 8 * I_MG; const int e = r / I_MG; r -= e * I_MG; W = a.in[up ? I_MWU : I_MWG] + (size_t)e * D * DFE; w.K = D; w.N = DFE;
;             w.dst = a.ws + WS_MGU_T + (size_t)e * 2 * DFE * D * (MOE_FP8 ? 1 : 2); w.kind = 2 + up; w.f8 = MOE_FP8; w.scale = F8_WGU; }
;         else { r -= 16 * I_MG; const int e = r / I_MD; r -= e * I_MD; W = a.in[I_MWD] + (size_t)e * DFE * D; w.K = DFE; w.N = D; w.dst = a.ws + WS_MD_T + (size_t)e * D * DFE * (MOE_FP8 ? 1 : 2); w.f8 = MOE_FP8; w.scale = F8_WD; }
;         const int nblk = (w.N + 31) >> 5, kb = r / nblk, nb = r - kb * nblk;
;         w.k0 = 128 * kb + 16 * (lane >> 3); w.n = 32 * nb + 4 * (lane & 7); w.valid = w.n < w.N; w.src = W + (size_t)w.k0 * w.N + w.n;
; __device__ __forceinline__ void nsa_unit(const Args& a, LAS unsigned char* lds, int b, int kvh, int qb) {
;     ...
; #pragma unroll
;     for (int dt = 0; dt < 4; ++dt)
; #pragma unroll
;         for (int i = 0; i < 16; ++i) o[dt][i] = 0.f;
;     float mrun = -1e30f, lrun = 0.f;
;     f32x16 p0, p1;
; #pragma unroll
;     for (int i = 0; i < 16; ++i) { p0[i] = 0.f; p1[i] = 0.f; }
;     bf16x8 pf[2][2];
;     if (w >= 4) asm volatile("s_barrier" ::: "memory");
; #pragma unroll 1
;     for (int it = 0; it <= nTot; ++it) {
.LBB0_1840:
	s_cmp_lt_i32 s17, -1
	s_cbranch_scc1 .LBB0_1865
	v_mov_b32_e32 v49, v47
	s_lshl_b32 s0, s62, 1
	s_max_i32 s1, s62, 8
	v_mov_b32_e32 v60, v47
	v_mov_b32_e32 v61, v47
	v_lshl_add_u64 v[206:207], s[30:31], 0, v[48:49]
	s_sub_i32 s69, s0, s1
	v_mov_b32_e32 v46, v47
	v_mov_b32_e32 v48, v47
	v_mov_b32_e32 v50, v47
	v_mov_b32_e32 v51, v47
	v_mov_b32_e32 v52, v47
	v_mov_b32_e32 v53, v47
	v_mov_b32_e32 v54, v47
	v_mov_b32_e32 v55, v47
	v_mov_b32_e32 v56, v47
	v_mov_b32_e32 v57, v47
	v_mov_b32_e32 v58, v47
	v_mov_b32_e32 v59, v47
	v_mov_b64_e32 v[108:109], v[60:61]
	v_mov_b64_e32 v[124:125], v[60:61]
	v_mov_b64_e32 v[140:141], v[60:61]
	v_mov_b64_e32 v[156:157], v[60:61]
	v_mov_b64_e32 v[76:77], v[60:61]
	v_mov_b64_e32 v[92:93], v[60:61]
	v_add_u32_e32 v43, 1, v249
	s_add_i32 s56, s69, 11
	s_add_i32 s57, s69, 10
	s_mov_b32 s68, 2
	s_add_i32 s69, s69, 2
	s_mov_b32 s70, 0
	v_mov_b32_e32 v208, 0xf149f2ca
	v_mov_b32_e32 v209, 0
	s_movk_i32 s71, 0xc000
	v_mov_b64_e32 v[106:107], v[58:59]
	v_mov_b64_e32 v[104:105], v[56:57]
	v_mov_b64_e32 v[102:103], v[54:55]
	v_mov_b64_e32 v[100:101], v[52:53]
	v_mov_b64_e32 v[98:99], v[50:51]
	v_mov_b64_e32 v[96:97], v[48:49]
	v_mov_b64_e32 v[94:95], v[46:47]
	v_mov_b64_e32 v[122:123], v[58:59]
	v_mov_b64_e32 v[120:121], v[56:57]
	v_mov_b64_e32 v[118:119], v[54:55]
	v_mov_b64_e32 v[116:117], v[52:53]
	v_mov_b64_e32 v[114:115], v[50:51]
	v_mov_b64_e32 v[112:113], v[48:49]
	v_mov_b64_e32 v[110:111], v[46:47]
	v_mov_b64_e32 v[138:139], v[58:59]
	v_mov_b64_e32 v[136:137], v[56:57]
	v_mov_b64_e32 v[134:135], v[54:55]
	v_mov_b64_e32 v[132:133], v[52:53]
	v_mov_b64_e32 v[130:131], v[50:51]
	v_mov_b64_e32 v[128:129], v[48:49]
	v_mov_b64_e32 v[126:127], v[46:47]
	v_mov_b64_e32 v[154:155], v[58:59]
	v_mov_b64_e32 v[152:153], v[56:57]
	v_mov_b64_e32 v[150:151], v[54:55]
	v_mov_b64_e32 v[148:149], v[52:53]
	v_mov_b64_e32 v[146:147], v[50:51]
	v_mov_b64_e32 v[144:145], v[48:49]
	v_mov_b64_e32 v[142:143], v[46:47]
	v_mov_b64_e32 v[74:75], v[58:59]
	v_mov_b64_e32 v[72:73], v[56:57]
	v_mov_b64_e32 v[70:71], v[54:55]
	v_mov_b64_e32 v[68:69], v[52:53]
	v_mov_b64_e32 v[66:67], v[50:51]
	v_mov_b64_e32 v[64:65], v[48:49]
	v_mov_b64_e32 v[62:63], v[46:47]
	v_mov_b64_e32 v[90:91], v[58:59]
	v_mov_b64_e32 v[88:89], v[56:57]
	v_mov_b64_e32 v[86:87], v[54:55]
	v_mov_b64_e32 v[84:85], v[52:53]
	v_mov_b64_e32 v[82:83], v[50:51]
	v_mov_b64_e32 v[80:81], v[48:49]
	v_mov_b64_e32 v[78:79], v[46:47]
	s_waitcnt vmcnt(0)
	s_and_b32 s14, s101, 0x7fffffff
	s_cmp_ge_u32 s14, 168
	s_cbranch_scc1 .Lcn_ldum_n1s
	s_and_b32 s14, s101, 0x7fffffff
	s_mul_i32 s15, s14, 0x2493
	s_lshr_b32 s15, s15, 16
	s_mul_i32 s67, s15, 7
	s_sub_u32 s67, s14, s67
	s_lshl_b32 s67, s67, 11
	s_add_u32 s67, s67, s100
	s_cmp_ge_u32 s15, 16
	s_cbranch_scc1 .Lcn_dn_n1ss
	s_lshr_b32 vcc_lo, s67, 5
	s_mul_i32 vcc_lo, vcc_lo, 0x2493
	s_lshr_b32 vcc_lo, vcc_lo, 16
	s_mul_i32 vcc_hi, vcc_lo, 0xe0
	s_sub_u32 vcc_hi, s67, vcc_hi
	s_and_b32 s67, s15, 1
	s_lshr_b32 s15, s15, 1
	s_mul_i32 s14, s15, 0x3800000
	s_mul_i32 s15, vcc_lo, 0xe0000
	s_add_u32 s14, s14, s15
	s_lshl_b32 s15, vcc_hi, 7
	s_add_u32 s14, s14, s15
	v_readlane_b32 s32, v255, 46
	v_readlane_b32 s33, v255, 47
	s_cmp_eq_u32 s67, 0
	s_cselect_b32 s32, s98, s32
	s_cselect_b32 s33, s99, s33
	s_add_u32 s32, s32, s14
	s_addc_u32 s33, s33, 0
	s_mov_b32 s1, 1
	s_branch .Lcn_dd_n1ss
.Lcn_dn_n1ss:
	s_sub_u32 s15, s15, 16
	s_lshr_b32 vcc_lo, s67, 6
	s_and_b32 vcc_hi, s67, 63
	s_mul_i32 s14, s15, 0x3800000
	s_lshl_b32 s15, vcc_lo, 18
	s_add_u32 s14, s14, s15
	s_lshl_b32 s15, vcc_hi, 7
	s_add_u32 s14, s14, s15
	v_readlane_b32 s32, v255, 48
	v_readlane_b32 s33, v255, 49
	s_add_u32 s32, s32, s14
	s_addc_u32 s33, s33, 0
	s_mov_b32 s1, 2

; __device__ __forceinline__ void witem_load(const WItem& w, f32x4 (&v)[16]) {
;     if (!w.valid) return;
; #pragma unroll
;     for (int i = 0; i < 16; ++i) v[i] = *(const f32x4*)(w.src + (size_t)i * w.N);
; __device__ __forceinline__ void nsa_unit(const Args& a, LAS unsigned char* lds, int b, int kvh, int qb) {
;     ...
; #pragma unroll 1
;     for (int it = 0; it <= nTot; ++it) {
;         if (it + 1 < nTot) asm volatile("s_waitcnt vmcnt(4) lgkmcnt(0)\n\ts_barrier" ::: "memory"); else asm volatile("s_waitcnt vmcnt(0) lgkmcnt(0)\n\ts_barrier" ::: "memory");
.Lcn_lgo_n1s:
	s_movk_i32 s14, 0x2000
	s_cmp_eq_u32 s1, 1
	s_cselect_b32 s14, 0x7000, s14
	v_and_b32_e32 v220, 63, v0
	v_and_b32_e32 v253, 7, v220
	v_lshrrev_b32_e32 v220, 3, v220
	v_lshlrev_b32_e32 v220, 2, v220
	v_lshlrev_b32_e32 v221, 4, v253
	v_lshlrev_b32_e32 v253, 2, v253
	v_mad_u32_u24 v254, v220, s14, v221
	global_load_dwordx4 v[212:215], v254, s[32:33] nt
	s_add_u32 s32, s32, s14
	s_addc_u32 s33, s33, 0
	global_load_dwordx4 v[216:219], v254, s[32:33] nt
	s_add_u32 s32, s32, s14
	s_addc_u32 s33, s33, 0
	global_load_dwordx4 v[224:227], v254, s[32:33] nt
	s_add_u32 s32, s32, s14
	s_addc_u32 s33, s33, 0
	global_load_dwordx2 v[220:221], v254, s[32:33] offset:0 nt
	global_load_dword v253, v254, s[32:33] offset:8 nt
	global_load_dword v254, v254, s[32:33] offset:12 nt
	s_branch .LBB0_1843
.LBB0_1842:
	s_add_i32 s14, s70, 2
	s_cmp_gt_i32 s14, s17
	s_cbranch_scc1 .Lcn_w0_n1
	s_waitcnt vmcnt(4)
	s_branch .Lcn_wd_n1

; __device__ __forceinline__ unsigned pk4_fp8(float a, float b, float c, float d) { int p = __builtin_amdgcn_cvt_pk_fp8_f32(a, b, 0, false); p = __builtin_amdgcn_cvt_pk_fp8_f32(c, d, p, true); return (unsigned)p; }
; __device__ __forceinline__ int witem_row(int kind, int n) {
;     if (kind == 1) return inproj_dst_row(n);
;     if (kind == 2) return ((n >> 7) << 8) + (n & 127);
;     if (kind == 3) return ((n >> 7) << 8) + 128 + (n & 127);
;     return n;
; }
; __device__ __forceinline__ void witem_load(const WItem& w, f32x4 (&v)[16]) {
;     if (!w.valid) return;
; #pragma unroll
;     for (int i = 0; i < 16; ++i) v[i] = *(const f32x4*)(w.src + (size_t)i * w.N);
; }
; __device__ __forceinline__ void witem_store(const WItem& w, const f32x4 (&v)[16]) {
;     if (!w.valid) return;
;     if (w.f8) {
; #pragma unroll
;         for (int j = 0; j < 4; ++j) { u32x4 o; const float sc = w.scale;
;             o.x = pk4_fp8(v[0][j] * sc, v[1][j] * sc, v[2][j] * sc, v[3][j] * sc); o.y = pk4_fp8(v[4][j] * sc, v[5][j] * sc, v[6][j] * sc, v[7][j] * sc);
;             o.z = pk4_fp8(v[8][j] * sc, v[9][j] * sc, v[10][j] * sc, v[11][j] * sc); o.w = pk4_fp8(v[12][j] * sc, v[13][j] * sc, v[14][j] * sc, v[15][j] * sc);
;             *(u32x4*)(w.dst + (size_t)witem_row(w.kind, w.n + j) * w.K + w.k0) = o; }
; __device__ __forceinline__ void p0_weights(const Args& a, LAS unsigned char* lds) {
;     ...
;         else if ((r -= I_FD) < 16 * I_MG) { const int up = r / (8 * I_MG); r -= up * 8 * I_MG; const int e = r / I_MG; r -= e * I_MG; W = a.in[up ? I_MWU : I_MWG] + (size_t)e * D * DFE; w.K = D; w.N = DFE;
;             w.dst = a.ws + WS_MGU_T + (size_t)e * 2 * DFE * D * (MOE_FP8 ? 1 : 2); w.kind = 2 + up; w.f8 = MOE_FP8; w.scale = F8_WGU; }
;         else { r -= 16 * I_MG; const int e = r / I_MD; r -= e * I_MD; W = a.in[I_MWD] + (size_t)e * DFE * D; w.K = DFE; w.N = D; w.dst = a.ws + WS_MD_T + (size_t)e * D * DFE * (MOE_FP8 ? 1 : 2); w.f8 = MOE_FP8; w.scale = F8_WD; }
;         const int nblk = (w.N + 31) >> 5, kb = r / nblk, nb = r - kb * nblk;
;         w.k0 = 128 * kb + 16 * (lane >> 3); w.n = 32 * nb + 4 * (lane & 7); w.valid = w.n < w.N; w.src = W + (size_t)w.k0 * w.N + w.n;
.Lcn_wd_n1:
	s_bitcmp1_b32 s101, 31
	s_cbranch_scc0 .Lcn_snone_n1l
	s_and_b32 s14, s101, 0x7fffffff
	s_sub_u32 s14, s14, 1
	s_mul_i32 s15, s14, 0x2493
	s_lshr_b32 s15, s15, 16
	s_mul_i32 s67, s15, 7
	s_sub_u32 s67, s14, s67
	s_lshl_b32 s67, s67, 11
	s_add_u32 s67, s67, s100
	s_cmp_ge_u32 s15, 16
	s_cbranch_scc1 .Lcn_dn_n1ld
	s_lshr_b32 vcc_lo, s67, 5
	s_mul_i32 vcc_lo, vcc_lo, 0x2493
	s_lshr_b32 vcc_lo, vcc_lo, 16
	s_mul_i32 vcc_hi, vcc_lo, 0xe0
	s_sub_u32 vcc_hi, s67, vcc_hi
	s_and_b32 s67, s15, 1
	s_lshr_b32 s15, s15, 1
	s_mul_i32 s14, s15, 0x1c00000
	s_add_u32 s14, s14, 0x4a000000
	s_lshr_b32 s15, vcc_hi, 2
	s_lshl_b32 s15, s15, 8
	s_lshl_b32 s67, s67, 7
	s_add_u32 s15, s15, s67
	s_and_b32 s67, vcc_hi, 3
	s_lshl_b32 s67, s67, 5
	s_add_u32 s15, s15, s67
	s_lshl_b32 s15, s15, 11
	s_add_u32 s14, s14, s15
	s_lshl_b32 s15, vcc_lo, 5
	s_add_u32 s14, s14, s15
	v_readlane_b32 s32, v255, 52
	v_readlane_b32 s33, v255, 53
	s_add_u32 s32, s32, s14
	s_addc_u32 s33, s33, 0
	s_mov_b32 s1, 1
	s_branch .Lcn_dd_n1ld
.Lcn_dn_n1ld:
	s_sub_u32 s15, s15, 16
	s_lshr_b32 vcc_lo, s67, 6
	s_and_b32 vcc_hi, s67, 63
	s_mul_i32 s14, s15, 0xe00000
	s_add_u32 s14, s14, 0x66000000
	s_mul_i32 s15, vcc_hi, 0x38000
	s_add_u32 s14, s14, s15
	s_lshl_b32 s15, vcc_lo, 5
	s_add_u32 s14, s14, s15
	v_readlane_b32 s32, v255, 52
	v_readlane_b32 s33, v255, 53
	s_add_u32 s32, s32, s14
	s_addc_u32 s33, s33, 0
	s_mov_b32 s1, 2
.Lcn_dd_n1ld:
	s_bitset0_b32 s101, 31
	s_mov_b32 s0, 0x42000000
	s_movk_i32 s14, 0x800
	s_cmp_eq_u32 s1, 2
	s_cselect_b32 s0, 0x43000000, s0
	s_cselect_b32 s14, 0x1c00, s14
	v_mul_f32_e32 v212, s0, v212
	v_mul_f32_e32 v213, s0, v213
	v_mul_f32_e32 v214, s0, v214
	v_mul_f32_e32 v215, s0, v215
	v_mul_f32_e32 v216, s0, v216
	v_mul_f32_e32 v217, s0, v217
	v_mul_f32_e32 v218, s0, v218
	v_mul_f32_e32 v219, s0, v219
	v_mul_f32_e32 v224, s0, v224
	v_mul_f32_e32 v225, s0, v225
	v_mul_f32_e32 v226, s0, v226
	v_mul_f32_e32 v227, s0, v227
	v_mul_f32_e32 v220, s0, v220
	v_mul_f32_e32 v221, s0, v221
	v_mul_f32_e32 v253, s0, v253
	v_mul_f32_e32 v254, s0, v254
	v_cvt_pk_fp8_f32 v212, v212, v216
	v_cvt_pk_fp8_f32 v213, v213, v217
	v_cvt_pk_fp8_f32 v214, v214, v218
	v_cvt_pk_fp8_f32 v215, v215, v219
	v_cvt_pk_fp8_f32 v212, v224, v220 op_sel:[0,0,1]
	v_cvt_pk_fp8_f32 v213, v225, v221 op_sel:[0,0,1]
	v_cvt_pk_fp8_f32 v214, v226, v253 op_sel:[0,0,1]
	v_cvt_pk_fp8_f32 v215, v227, v254 op_sel:[0,0,1]
	v_and_b32_e32 v216, 63, v0
	v_and_b32_e32 v218, 7, v216
	v_lshrrev_b32_e32 v216, 3, v216
	v_lshlrev_b32_e32 v216, 2, v216
	v_lshlrev_b32_e32 v217, 4, v218
	v_lshlrev_b32_e32 v218, 2, v218
	v_mad_u32_u24 v217, v218, s14, v216
	global_store_dword v217, v212, s[32:33] nt
	v_add_u32_e32 v216, s14, v217
	global_store_dword v216, v213, s[32:33] nt
	v_add_u32_e32 v218, s14, v216
	global_store_dword v218, v214, s[32:33] nt
	v_add_u32_e32 v219, s14, v218
	global_store_dword v219, v215, s[32:33] nt
.Lcn_snone_n1l:
	s_and_b32 s14, s101, 0x7fffffff
	s_cmp_ge_u32 s14, 168
	s_cbranch_scc1 .Lcn_ldum_n1l
	s_and_b32 s14, s101, 0x7fffffff
	s_mul_i32 s15, s14, 0x2493
	s_lshr_b32 s15, s15, 16
	s_mul_i32 s67, s15, 7
	s_sub_u32 s67, s14, s67
	s_lshl_b32 s67, s67, 11
	s_add_u32 s67, s67, s100
	s_cmp_ge_u32 s15, 16
	s_cbranch_scc1 .Lcn_dn_n1ls
	s_lshr_b32 vcc_lo, s67, 5
	s_mul_i32 vcc_lo, vcc_lo, 0x2493
	s_lshr_b32 vcc_lo, vcc_lo, 16
	s_mul_i32 vcc_hi, vcc_lo, 0xe0
	s_sub_u32 vcc_hi, s67, vcc_hi
	s_and_b32 s67, s15, 1
	s_lshr_b32 s15, s15, 1
	s_mul_i32 s14, s15, 0x3800000
	s_mul_i32 s15, vcc_lo, 0xe0000
	s_add_u32 s14, s14, s15
	s_lshl_b32 s15, vcc_hi, 7
	s_add_u32 s14, s14, s15
	v_readlane_b32 s32, v255, 46
	v_readlane_b32 s33, v255, 47
	s_cmp_eq_u32 s67, 0
	s_cselect_b32 s32, s98, s32
	s_cselect_b32 s33, s99, s33
	s_add_u32 s32, s32, s14
	s_addc_u32 s33, s33, 0
	s_mov_b32 s1, 1
	s_branch .Lcn_dd_n1ls

; __device__ __forceinline__ void witem_load(const WItem& w, f32x4 (&v)[16]) {
;     if (!w.valid) return;
; #pragma unroll
;     for (int i = 0; i < 16; ++i) v[i] = *(const f32x4*)(w.src + (size_t)i * w.N);
; __device__ __forceinline__ void nsa_unit(const Args& a, LAS unsigned char* lds, int b, int kvh, int qb) {
;     ...
; #pragma unroll 1
;     for (int it = 0; it <= nTot; ++it) {
;         if (it + 1 < nTot) asm volatile("s_waitcnt vmcnt(4) lgkmcnt(0)\n\ts_barrier" ::: "memory"); else asm volatile("s_waitcnt vmcnt(0) lgkmcnt(0)\n\ts_barrier" ::: "memory");
.Lcn_lgo_n1l:
	s_movk_i32 s14, 0x2000
	s_cmp_eq_u32 s1, 1
	s_cselect_b32 s14, 0x7000, s14
	v_and_b32_e32 v220, 63, v0
	v_and_b32_e32 v253, 7, v220
	v_lshrrev_b32_e32 v220, 3, v220
	v_lshlrev_b32_e32 v220, 2, v220
	v_lshlrev_b32_e32 v221, 4, v253
	v_lshlrev_b32_e32 v253, 2, v253
	v_mad_u32_u24 v254, v220, s14, v221
	global_load_dwordx4 v[212:215], v254, s[32:33] nt
	s_add_u32 s32, s32, s14
	s_addc_u32 s33, s33, 0
	global_load_dwordx4 v[216:219], v254, s[32:33] nt
	s_add_u32 s32, s32, s14
	s_addc_u32 s33, s33, 0
	global_load_dwordx4 v[224:227], v254, s[32:33] nt
	s_add_u32 s32, s32, s14
	s_addc_u32 s33, s33, 0
	global_load_dwordx2 v[220:221], v254, s[32:33] offset:0 nt
	global_load_dword v253, v254, s[32:33] offset:8 nt
	global_load_dword v254, v254, s[32:33] offset:12 nt
	s_add_i32 s70, s70, 1
	s_addk_i32 s71, 0x4000
	s_add_i32 s68, s68, 1
	s_cmp_eq_u32 s56, s70
	s_cbranch_scc1 .LBB0_1865
.LBB0_1843:
	s_cmp_ge_i32 s70, s17
	s_mov_b64 s[0:1], -1
	s_cbranch_scc0 .LBB0_1846
	s_waitcnt vmcnt(10) lgkmcnt(0)
	s_barrier
	s_cbranch_execz .LBB0_1847

; __device__ __forceinline__ void nsa_unit(const Args& a, LAS unsigned char* lds, int b, int kvh, int qb) {
;     ...
;         if (it + 1 < nTot) asm volatile("s_waitcnt vmcnt(4) lgkmcnt(0)\n\ts_barrier" ::: "memory"); else asm volatile("s_waitcnt vmcnt(0) lgkmcnt(0)\n\ts_barrier" ::: "memory");
.LBB0_1847:
	s_waitcnt vmcnt(14) lgkmcnt(0)
	s_barrier
	s_cmp_lg_u32 s70, 0
	s_cselect_b64 s[0:1], -1, 0
	s_cmp_eq_u32 s70, 0
	s_cbranch_scc1 .LBB0_1858

; #define GAS __attribute__((address_space(1)))
; #define LAS __attribute__((address_space(3)))
; __device__ __forceinline__ unsigned cvt_pk_bf16(float lo, float hi) { unsigned r; asm volatile("v_cvt_pk_bf16_f32 %0, %1, %2" : "=v"(r) : "v"(lo), "v"(hi)); return r; }
; __device__ __forceinline__ void nsa_pv_rd4(const LAS unsigned char* vA, int sv, int step, bf16x8 (&af)[4]) {
; #pragma unroll
;     for (int dt = 0; dt < 4; ++dt) af[dt] = *(const LAS bf16x8*)(vA + dt * 4096 + (((2 * step) * 16) ^ sv));
; }
; __device__ __forceinline__ void nsa_pv_mm4(const bf16x8 (&af)[4], const bf16x8& pfk, f32x16 (&o)[4]) {
; #pragma unroll
;     for (int dt = 0; dt < 4; ++dt) o[dt] = __builtin_amdgcn_mfma_f32_32x32x16_bf16(af[dt], pfk, o[dt], 0, 0, 0);
; }
; __device__ __forceinline__ void nsa_pv_sw(const LAS unsigned char* vbuf, const bf16x8 (&pf)[2][2], f32x16 (&o)[4], int r, int h) {
;     const int sv = (((r >> 1) & 7) ^ h) * 16; const LAS unsigned char* vA = vbuf + r * 128;
; #pragma unroll
;     for (int step = 0; step < 4; ++step) { bf16x8 fa[4];
;         nsa_pv_rd4(vA, sv, step, fa); __builtin_amdgcn_sched_barrier(0);
;         nsa_pv_mm4(fa, pf[step >> 1][step & 1], o); __builtin_amdgcn_sched_barrier(0); }
; }
; __device__ __forceinline__ void nsa_unit(const Args& a, LAS unsigned char* lds, int b, int kvh, int qb) {
;     ...
;             if (ti == nS - 1 || ti == nTot - 1) {
;                 const float lt = lrun + __shfl_xor(lrun, 32); const float f = ((ti == nS - 1) ? g1 : g2) / lt;
; #pragma unroll
;                 for (int dt = 0; dt < 4; ++dt) {
; #pragma unroll
;                     for (int aa = 0; aa < 4; ++aa) { const u32x2 pv = *(const GAS u32x2*)(mp + (32 * dt + 8 * aa) * 2); u32x2 wv;
;                         wv.x = pg8::cvt_pk_bf16(bflo(pv.x) + o[dt][4 * aa] * f, bfhi(pv.x) + o[dt][4 * aa + 1] * f); wv.y = pg8::cvt_pk_bf16(bflo(pv.y) + o[dt][4 * aa + 2] * f, bfhi(pv.y) + o[dt][4 * aa + 3] * f);
;                         *(GAS u32x2*)(mp + (32 * dt + 8 * aa) * 2) = wv; }
.LBB0_1860:
	v_mov_b32_e32 v210, v222
	v_mov_b32_e32 v211, v45
	s_andn2_b64 vcc, exec, s[0:1]
	s_cbranch_vccnz .LBB0_1863
	s_and_b32 s0, s71, 0xc000
	v_lshrrev_b32_e32 v34, 1, v210
	s_add_i32 s0, s0, 0
	v_bitop3_b32 v34, v34, v211, 7 bitop3:0x6c
	v_lshlrev_b32_e32 v46, 4, v34
	v_lshl_add_u32 v56, v210, 7, s0
	v_add_u32_e32 v52, v56, v46
	ds_read_b128 v[34:37], v52 offset:49152
	ds_read_b128 v[38:41], v52 offset:53248
	ds_read_b128 v[48:51], v52 offset:57344
	ds_read_b128 v[52:55], v52 offset:61440
	s_waitcnt lgkmcnt(3)
	v_mfma_f32_32x32x16_bf16 v[142:157], v[34:37], v[190:193], v[142:157]
	s_waitcnt lgkmcnt(2)
	v_mfma_f32_32x32x16_bf16 v[126:141], v[38:41], v[190:193], v[126:141]
	s_waitcnt lgkmcnt(1)
	v_mfma_f32_32x32x16_bf16 v[110:125], v[48:51], v[190:193], v[110:125]
	s_waitcnt lgkmcnt(0)
	v_mfma_f32_32x32x16_bf16 v[94:109], v[52:55], v[190:193], v[94:109]
	v_xad_u32 v52, v46, 32, v56
	ds_read_b128 v[34:37], v52 offset:49152
	ds_read_b128 v[38:41], v52 offset:53248
	ds_read_b128 v[48:51], v52 offset:57344
	ds_read_b128 v[52:55], v52 offset:61440
	s_waitcnt lgkmcnt(3)
	v_mfma_f32_32x32x16_bf16 v[142:157], v[34:37], v[194:197], v[142:157]
	s_waitcnt lgkmcnt(2)
	v_mfma_f32_32x32x16_bf16 v[126:141], v[38:41], v[194:197], v[126:141]
	s_waitcnt lgkmcnt(1)
	v_mfma_f32_32x32x16_bf16 v[110:125], v[48:51], v[194:197], v[110:125]
	s_waitcnt lgkmcnt(0)
	v_mfma_f32_32x32x16_bf16 v[94:109], v[52:55], v[194:197], v[94:109]
	v_xad_u32 v52, v46, 64, v56
	ds_read_b128 v[34:37], v52 offset:49152
	ds_read_b128 v[38:41], v52 offset:53248
	ds_read_b128 v[48:51], v52 offset:57344
	ds_read_b128 v[52:55], v52 offset:61440
	s_waitcnt lgkmcnt(3)
	v_mfma_f32_32x32x16_bf16 v[142:157], v[34:37], v[198:201], v[142:157]
	s_waitcnt lgkmcnt(2)
	v_mfma_f32_32x32x16_bf16 v[126:141], v[38:41], v[198:201], v[126:141]
	s_waitcnt lgkmcnt(1)
	v_mfma_f32_32x32x16_bf16 v[110:125], v[48:51], v[198:201], v[110:125]
	s_waitcnt lgkmcnt(0)
	v_mfma_f32_32x32x16_bf16 v[94:109], v[52:55], v[198:201], v[94:109]
	v_xad_u32 v46, v46, s60, v56
	ds_read_b128 v[34:37], v46 offset:49152
	ds_read_b128 v[38:41], v46 offset:53248
	ds_read_b128 v[48:51], v46 offset:57344
	ds_read_b128 v[52:55], v46 offset:61440
	s_waitcnt lgkmcnt(3)
	v_mfma_f32_32x32x16_bf16 v[142:157], v[34:37], v[202:205], v[142:157]
	s_waitcnt lgkmcnt(2)
	v_mfma_f32_32x32x16_bf16 v[126:141], v[38:41], v[202:205], v[126:141]
	s_waitcnt lgkmcnt(1)
	v_mfma_f32_32x32x16_bf16 v[110:125], v[48:51], v[202:205], v[110:125]
	s_waitcnt lgkmcnt(0)
	v_mfma_f32_32x32x16_bf16 v[94:109], v[52:55], v[202:205], v[94:109]
	s_cmp_eq_u32 s16, s70
	s_cselect_b64 s[12:13], -1, 0
	s_cmp_eq_u32 s57, s70
	s_cselect_b64 s[0:1], -1, 0
	s_or_b64 s[0:1], s[12:13], s[0:1]
	s_andn2_b64 vcc, exec, s[0:1]
	s_cbranch_vccnz .LBB0_1863
	ds_bpermute_b32 v233, v252, v209
	v_cndmask_b32_e64 v208, v251, v250, s[12:13]
	v_mov_b32_e32 v60, v47
	v_mov_b32_e32 v61, v47
	v_mov_b32_e32 v48, v47
	s_waitcnt lgkmcnt(0)
	v_pk_add_f32 v[34:35], v[208:209], v[232:233]
	v_mov_b32_e32 v49, v47
	v_div_scale_f32 v36, s[0:1], v34, v34, 1.0
	v_rcp_f32_e32 v37, v36
	v_mov_b32_e32 v50, v47
	v_mov_b32_e32 v51, v47
	v_mov_b32_e32 v52, v47
	v_fma_f32 v38, -v36, v37, 1.0
	v_fmac_f32_e32 v37, v38, v37
	v_div_scale_f32 v38, vcc, 1.0, v34, 1.0
	v_mul_f32_e32 v39, v38, v37
	v_fma_f32 v40, -v36, v39, v38
	v_fmac_f32_e32 v39, v40, v37
	v_fma_f32 v36, -v36, v39, v38
	v_div_fmas_f32 v36, v36, v37, v39
	v_div_fixup_f32 v34, v36, v34, 1.0
	v_div_scale_f32 v36, s[0:1], v35, v35, v34
	v_rcp_f32_e32 v37, v36
	v_mov_b32_e32 v53, v47
	v_mov_b32_e32 v54, v47
	v_mov_b32_e32 v55, v47
	v_fma_f32 v38, -v36, v37, 1.0
	v_fmac_f32_e32 v37, v38, v37
	v_div_scale_f32 v38, vcc, v34, v35, v34
	v_mul_f32_e32 v39, v38, v37
	v_fma_f32 v40, -v36, v39, v38
	v_fmac_f32_e32 v39, v40, v37
	v_fma_f32 v36, -v36, v39, v38
	v_div_fmas_f32 v36, v36, v37, v39
	v_div_fixup_f32 v46, v36, v35, v34
	v_mov_b32_e32 v56, v47
	v_mov_b32_e32 v57, v47
	v_mov_b32_e32 v58, v47
	v_mov_b32_e32 v59, v47
	v_mov_b32_e32 v208, 0xf149f2ca
	v_mov_b32_e32 v209, 0
	global_load_dwordx2 v[62:63], v[206:207], off
	global_load_dwordx2 v[64:65], v[206:207], off offset:16
	global_load_dwordx2 v[66:67], v[206:207], off offset:32
	global_load_dwordx2 v[68:69], v[206:207], off offset:48
	global_load_dwordx2 v[70:71], v[206:207], off offset:64
	global_load_dwordx2 v[72:73], v[206:207], off offset:80
	global_load_dwordx2 v[74:75], v[206:207], off offset:96
	global_load_dwordx2 v[76:77], v[206:207], off offset:112
	global_load_dwordx2 v[78:79], v[206:207], off offset:128
	global_load_dwordx2 v[80:81], v[206:207], off offset:144
	global_load_dwordx2 v[82:83], v[206:207], off offset:160
	global_load_dwordx2 v[84:85], v[206:207], off offset:176
	global_load_dwordx2 v[86:87], v[206:207], off offset:192
	global_load_dwordx2 v[88:89], v[206:207], off offset:208
	global_load_dwordx2 v[90:91], v[206:207], off offset:224
	global_load_dwordx2 v[92:93], v[206:207], off offset:240
	s_waitcnt vmcnt(15)
	v_lshlrev_b32_e32 v36, 16, v62
	v_and_b32_e32 v34, 0xffff0000, v62
	v_fmac_f32_e32 v36, v142, v46
	v_fmac_f32_e32 v34, v143, v46
	v_cvt_pk_bf16_f32 v34, v36, v34
	v_lshlrev_b32_e32 v36, 16, v63
	v_and_b32_e32 v35, 0xffff0000, v63
	v_fmac_f32_e32 v35, v145, v46
	v_fmac_f32_e32 v36, v144, v46
	v_cvt_pk_bf16_f32 v35, v36, v35
	global_store_dwordx2 v[206:207], v[34:35], off
	s_waitcnt vmcnt(15)
	v_lshlrev_b32_e32 v36, 16, v64
	v_and_b32_e32 v34, 0xffff0000, v64
	v_fmac_f32_e32 v36, v146, v46
	v_fmac_f32_e32 v34, v147, v46
	v_cvt_pk_bf16_f32 v34, v36, v34
	v_lshlrev_b32_e32 v36, 16, v65
	v_and_b32_e32 v35, 0xffff0000, v65
	v_fmac_f32_e32 v35, v149, v46
	v_fmac_f32_e32 v36, v148, v46
	v_cvt_pk_bf16_f32 v35, v36, v35
	global_store_dwordx2 v[206:207], v[34:35], off offset:16
	s_waitcnt vmcnt(15)
; #define GAS __attribute__((address_space(1)))
; __device__ __forceinline__ unsigned cvt_pk_bf16(float lo, float hi) { unsigned r; asm volatile("v_cvt_pk_bf16_f32 %0, %1, %2" : "=v"(r) : "v"(lo), "v"(hi)); return r; }
; __device__ __forceinline__ void nsa_unit(const Args& a, LAS unsigned char* lds, int b, int kvh, int qb) {
;     ...
;                 const float lt = lrun + __shfl_xor(lrun, 32); const float f = ((ti == nS - 1) ? g1 : g2) / lt;
; #pragma unroll
;                 for (int dt = 0; dt < 4; ++dt) {
; #pragma unroll
;                     for (int aa = 0; aa < 4; ++aa) { const u32x2 pv = *(const GAS u32x2*)(mp + (32 * dt + 8 * aa) * 2); u32x2 wv;
;                         wv.x = pg8::cvt_pk_bf16(bflo(pv.x) + o[dt][4 * aa] * f, bfhi(pv.x) + o[dt][4 * aa + 1] * f); wv.y = pg8::cvt_pk_bf16(bflo(pv.y) + o[dt][4 * aa + 2] * f, bfhi(pv.y) + o[dt][4 * aa + 3] * f);
;                         *(GAS u32x2*)(mp + (32 * dt + 8 * aa) * 2) = wv; }
; #pragma unroll
;                     for (int i = 0; i < 16; ++i) o[dt][i] = 0.f; }
;                 mrun = -1e30f; lrun = 0.f;
	v_lshlrev_b32_e32 v36, 16, v66
	v_and_b32_e32 v34, 0xffff0000, v66
	v_fmac_f32_e32 v36, v150, v46
	v_fmac_f32_e32 v34, v151, v46
	v_cvt_pk_bf16_f32 v34, v36, v34
	v_lshlrev_b32_e32 v36, 16, v67
	v_and_b32_e32 v35, 0xffff0000, v67
	v_fmac_f32_e32 v35, v153, v46
	v_fmac_f32_e32 v36, v152, v46
	v_cvt_pk_bf16_f32 v35, v36, v35
	global_store_dwordx2 v[206:207], v[34:35], off offset:32
	s_waitcnt vmcnt(15)
	v_lshlrev_b32_e32 v36, 16, v68
	v_and_b32_e32 v34, 0xffff0000, v68
	v_fmac_f32_e32 v36, v154, v46
	v_fmac_f32_e32 v34, v155, v46
	v_cvt_pk_bf16_f32 v34, v36, v34
	v_lshlrev_b32_e32 v36, 16, v69
	v_and_b32_e32 v35, 0xffff0000, v69
	v_fmac_f32_e32 v35, v157, v46
	v_fmac_f32_e32 v36, v156, v46
	v_cvt_pk_bf16_f32 v35, v36, v35
	global_store_dwordx2 v[206:207], v[34:35], off offset:48
	s_waitcnt vmcnt(15)
	v_lshlrev_b32_e32 v36, 16, v70
	v_and_b32_e32 v34, 0xffff0000, v70
	v_fmac_f32_e32 v36, v126, v46
	v_fmac_f32_e32 v34, v127, v46
	v_cvt_pk_bf16_f32 v34, v36, v34
	v_lshlrev_b32_e32 v36, 16, v71
	v_and_b32_e32 v35, 0xffff0000, v71
	v_fmac_f32_e32 v35, v129, v46
	v_fmac_f32_e32 v36, v128, v46
	v_cvt_pk_bf16_f32 v35, v36, v35
	global_store_dwordx2 v[206:207], v[34:35], off offset:64
	s_waitcnt vmcnt(15)
	v_lshlrev_b32_e32 v36, 16, v72
	v_and_b32_e32 v34, 0xffff0000, v72
	v_fmac_f32_e32 v36, v130, v46
	v_fmac_f32_e32 v34, v131, v46
	v_cvt_pk_bf16_f32 v34, v36, v34
	v_lshlrev_b32_e32 v36, 16, v73
	v_and_b32_e32 v35, 0xffff0000, v73
	v_fmac_f32_e32 v35, v133, v46
	v_fmac_f32_e32 v36, v132, v46
	v_cvt_pk_bf16_f32 v35, v36, v35
	global_store_dwordx2 v[206:207], v[34:35], off offset:80
	s_waitcnt vmcnt(15)
	v_lshlrev_b32_e32 v36, 16, v74
	v_and_b32_e32 v34, 0xffff0000, v74
	v_fmac_f32_e32 v36, v134, v46
	v_fmac_f32_e32 v34, v135, v46
	v_cvt_pk_bf16_f32 v34, v36, v34
	v_lshlrev_b32_e32 v36, 16, v75
	v_and_b32_e32 v35, 0xffff0000, v75
	v_fmac_f32_e32 v35, v137, v46
	v_fmac_f32_e32 v36, v136, v46
	v_cvt_pk_bf16_f32 v35, v36, v35
	global_store_dwordx2 v[206:207], v[34:35], off offset:96
	s_waitcnt vmcnt(15)
	v_lshlrev_b32_e32 v36, 16, v76
	v_and_b32_e32 v34, 0xffff0000, v76
	v_fmac_f32_e32 v36, v138, v46
	v_fmac_f32_e32 v34, v139, v46
	v_cvt_pk_bf16_f32 v34, v36, v34
	v_lshlrev_b32_e32 v36, 16, v77
	v_and_b32_e32 v35, 0xffff0000, v77
	v_fmac_f32_e32 v35, v141, v46
	v_fmac_f32_e32 v36, v140, v46
	v_cvt_pk_bf16_f32 v35, v36, v35
	global_store_dwordx2 v[206:207], v[34:35], off offset:112
	s_waitcnt vmcnt(15)
	v_lshlrev_b32_e32 v36, 16, v78
	v_and_b32_e32 v34, 0xffff0000, v78
	v_fmac_f32_e32 v36, v110, v46
	v_fmac_f32_e32 v34, v111, v46
	v_cvt_pk_bf16_f32 v34, v36, v34
	v_lshlrev_b32_e32 v36, 16, v79
	v_and_b32_e32 v35, 0xffff0000, v79
	v_fmac_f32_e32 v35, v113, v46
	v_fmac_f32_e32 v36, v112, v46
	v_cvt_pk_bf16_f32 v35, v36, v35
	global_store_dwordx2 v[206:207], v[34:35], off offset:128
	s_waitcnt vmcnt(15)
	v_lshlrev_b32_e32 v36, 16, v80
	v_and_b32_e32 v34, 0xffff0000, v80
	v_fmac_f32_e32 v36, v114, v46
	v_fmac_f32_e32 v34, v115, v46
	v_cvt_pk_bf16_f32 v34, v36, v34
	v_lshlrev_b32_e32 v36, 16, v81
	v_and_b32_e32 v35, 0xffff0000, v81
	v_fmac_f32_e32 v35, v117, v46
	v_fmac_f32_e32 v36, v116, v46
	v_cvt_pk_bf16_f32 v35, v36, v35
	global_store_dwordx2 v[206:207], v[34:35], off offset:144
	s_waitcnt vmcnt(15)
	v_lshlrev_b32_e32 v36, 16, v82
	v_and_b32_e32 v34, 0xffff0000, v82
	v_fmac_f32_e32 v36, v118, v46
	v_fmac_f32_e32 v34, v119, v46
	v_cvt_pk_bf16_f32 v34, v36, v34
	v_lshlrev_b32_e32 v36, 16, v83
	v_and_b32_e32 v35, 0xffff0000, v83
	v_fmac_f32_e32 v35, v121, v46
	v_fmac_f32_e32 v36, v120, v46
	v_cvt_pk_bf16_f32 v35, v36, v35
	global_store_dwordx2 v[206:207], v[34:35], off offset:160
	s_waitcnt vmcnt(15)
	v_lshlrev_b32_e32 v36, 16, v84
	v_and_b32_e32 v34, 0xffff0000, v84
	v_fmac_f32_e32 v36, v122, v46
	v_fmac_f32_e32 v34, v123, v46
	v_cvt_pk_bf16_f32 v34, v36, v34
	v_lshlrev_b32_e32 v36, 16, v85
	v_and_b32_e32 v35, 0xffff0000, v85
	v_fmac_f32_e32 v35, v125, v46
	v_fmac_f32_e32 v36, v124, v46
	v_cvt_pk_bf16_f32 v35, v36, v35
	global_store_dwordx2 v[206:207], v[34:35], off offset:176
	s_waitcnt vmcnt(15)
	v_lshlrev_b32_e32 v36, 16, v86
	v_and_b32_e32 v34, 0xffff0000, v86
	v_fmac_f32_e32 v36, v94, v46
	v_fmac_f32_e32 v34, v95, v46
	v_cvt_pk_bf16_f32 v34, v36, v34
	v_lshlrev_b32_e32 v36, 16, v87
	v_and_b32_e32 v35, 0xffff0000, v87
	v_fmac_f32_e32 v35, v97, v46
	v_fmac_f32_e32 v36, v96, v46
	v_cvt_pk_bf16_f32 v35, v36, v35
	global_store_dwordx2 v[206:207], v[34:35], off offset:192
	s_waitcnt vmcnt(15)
	v_lshlrev_b32_e32 v36, 16, v88
	v_and_b32_e32 v34, 0xffff0000, v88
	v_fmac_f32_e32 v36, v98, v46
	v_fmac_f32_e32 v34, v99, v46
	v_cvt_pk_bf16_f32 v34, v36, v34
	v_lshlrev_b32_e32 v36, 16, v89
	v_and_b32_e32 v35, 0xffff0000, v89
	v_fmac_f32_e32 v35, v101, v46
	v_fmac_f32_e32 v36, v100, v46
	v_cvt_pk_bf16_f32 v35, v36, v35
	global_store_dwordx2 v[206:207], v[34:35], off offset:208
	s_waitcnt vmcnt(15)
	v_lshlrev_b32_e32 v36, 16, v90
	v_and_b32_e32 v34, 0xffff0000, v90
	v_fmac_f32_e32 v36, v102, v46
	v_fmac_f32_e32 v34, v103, v46
	v_cvt_pk_bf16_f32 v34, v36, v34
	v_lshlrev_b32_e32 v36, 16, v91
	v_and_b32_e32 v35, 0xffff0000, v91
	v_fmac_f32_e32 v35, v105, v46
	v_fmac_f32_e32 v36, v104, v46
	v_cvt_pk_bf16_f32 v35, v36, v35
	global_store_dwordx2 v[206:207], v[34:35], off offset:224
	s_waitcnt vmcnt(15)
	v_lshlrev_b32_e32 v36, 16, v92
	v_and_b32_e32 v34, 0xffff0000, v92
	v_fmac_f32_e32 v36, v106, v46
	v_fmac_f32_e32 v34, v107, v46
	v_cvt_pk_bf16_f32 v34, v36, v34
	v_lshlrev_b32_e32 v36, 16, v93
	v_and_b32_e32 v35, 0xffff0000, v93
	v_fmac_f32_e32 v35, v109, v46
	v_fmac_f32_e32 v36, v108, v46
	v_cvt_pk_bf16_f32 v35, v36, v35
	global_store_dwordx2 v[206:207], v[34:35], off offset:240
	s_waitcnt vmcnt(0)
	v_mov_b32_e32 v46, v47
	v_mov_b64_e32 v[156:157], v[60:61]
	v_mov_b64_e32 v[140:141], v[60:61]
	v_mov_b64_e32 v[124:125], v[60:61]
	v_mov_b64_e32 v[108:109], v[60:61]
	v_mov_b64_e32 v[154:155], v[58:59]
	v_mov_b64_e32 v[152:153], v[56:57]
	v_mov_b64_e32 v[150:151], v[54:55]
	v_mov_b64_e32 v[148:149], v[52:53]
	v_mov_b64_e32 v[146:147], v[50:51]
	v_mov_b64_e32 v[144:145], v[48:49]
	v_mov_b64_e32 v[142:143], v[46:47]
	v_mov_b64_e32 v[138:139], v[58:59]
	v_mov_b64_e32 v[136:137], v[56:57]
	v_mov_b64_e32 v[134:135], v[54:55]
	v_mov_b64_e32 v[132:133], v[52:53]
	v_mov_b64_e32 v[130:131], v[50:51]
	v_mov_b64_e32 v[128:129], v[48:49]
	v_mov_b64_e32 v[126:127], v[46:47]
	v_mov_b64_e32 v[122:123], v[58:59]
	v_mov_b64_e32 v[120:121], v[56:57]
	v_mov_b64_e32 v[118:119], v[54:55]
	v_mov_b64_e32 v[116:117], v[52:53]
	v_mov_b64_e32 v[114:115], v[50:51]
	v_mov_b64_e32 v[112:113], v[48:49]
	v_mov_b64_e32 v[110:111], v[46:47]
	v_mov_b64_e32 v[106:107], v[58:59]
	v_mov_b64_e32 v[104:105], v[56:57]
	v_mov_b64_e32 v[102:103], v[54:55]
	v_mov_b64_e32 v[100:101], v[52:53]
	v_mov_b64_e32 v[98:99], v[50:51]
	v_mov_b64_e32 v[96:97], v[48:49]
	v_mov_b64_e32 v[94:95], v[46:47]
; #define LAS __attribute__((address_space(3)))
; __device__ __forceinline__ void p0_weights(const Args& a, LAS unsigned char* lds) {
;     ...
;         else if ((r -= I_FD) < 16 * I_MG) { const int up = r / (8 * I_MG); r -= up * 8 * I_MG; const int e = r / I_MG; r -= e * I_MG; W = a.in[up ? I_MWU : I_MWG] + (size_t)e * D * DFE; w.K = D; w.N = DFE;
;             w.dst = a.ws + WS_MGU_T + (size_t)e * 2 * DFE * D * (MOE_FP8 ? 1 : 2); w.kind = 2 + up; w.f8 = MOE_FP8; w.scale = F8_WGU; }
;         else { r -= 16 * I_MG; const int e = r / I_MD; r -= e * I_MD; W = a.in[I_MWD] + (size_t)e * DFE * D; w.K = DFE; w.N = D; w.dst = a.ws + WS_MD_T + (size_t)e * D * DFE * (MOE_FP8 ? 1 : 2); w.f8 = MOE_FP8; w.scale = F8_WD; }
;         const int nblk = (w.N + 31) >> 5, kb = r / nblk, nb = r - kb * nblk;
;         w.k0 = 128 * kb + 16 * (lane >> 3); w.n = 32 * nb + 4 * (lane & 7); w.valid = w.n < w.N; w.src = W + (size_t)w.k0 * w.N + w.n;
; __device__ __forceinline__ void nsa_qk_sw(const LAS unsigned char* kbuf, const bf16x8 (&qf)[8], int r, int h, f32x16& p0, f32x16& p1) {
;     const int x = r & 15; const LAS unsigned char* kA = kbuf + r * 256 + ((h ^ (x & 1)) * 16); const int xk = (x & 14) * 16;
; #pragma unroll
;     for (int i = 0; i < 16; ++i) { p0[i] = 0.f; p1[i] = 0.f; }
;     bf16x8 a0, a1, b0, b1;
;     a0 = *(const LAS bf16x8*)(kA + (0 ^ xk)); a1 = *(const LAS bf16x8*)(kA + (0 ^ xk) + 8192); __builtin_amdgcn_sched_barrier(0);
; #pragma unroll
;     for (int ks = 0; ks < 8; ks += 2) {
;         b0 = *(const LAS bf16x8*)(kA + (((ks + 1) * 32) ^ xk)); b1 = *(const LAS bf16x8*)(kA + (((ks + 1) * 32) ^ xk) + 8192); __builtin_amdgcn_sched_barrier(0);
;         p0 = __builtin_amdgcn_mfma_f32_32x32x16_bf16(a0, qf[ks], p0, 0, 0, 0); p1 = __builtin_amdgcn_mfma_f32_32x32x16_bf16(a1, qf[ks], p1, 0, 0, 0); __builtin_amdgcn_sched_barrier(0);
;         if (ks + 2 < 8) { a0 = *(const LAS bf16x8*)(kA + (((ks + 2) * 32) ^ xk)); a1 = *(const LAS bf16x8*)(kA + (((ks + 2) * 32) ^ xk) + 8192); } __builtin_amdgcn_sched_barrier(0);
;         p0 = __builtin_amdgcn_mfma_f32_32x32x16_bf16(b0, qf[ks + 1], p0, 0, 0, 0); p1 = __builtin_amdgcn_mfma_f32_32x32x16_bf16(b1, qf[ks + 1], p1, 0, 0, 0); __builtin_amdgcn_sched_barrier(0);
;     }
; }
.LBB0_1863:
	s_cmp_gt_i32 s70, s17
	s_cbranch_scc1 .LBB0_1842
	s_mul_hi_u32 s0, s70, 0xaaaaaaab
	s_lshr_b32 s0, s0, 1
	v_lshlrev_b32_e32 v57, 4, v210
	s_mul_i32 s0, s0, 0xffff4000
	v_lshlrev_b32_e32 v46, 8, v210
	v_bitop3_b32 v34, v210, v211, 1 bitop3:0x6c
	v_and_b32_e32 v58, 0xe0, v57
	s_add_i32 s1, s71, 0
	v_lshlrev_b32_e32 v56, 4, v34
	v_or_b32_e32 v34, v46, v58
	s_add_i32 s1, s1, s0
	v_add3_u32 v38, v34, v56, s1
	ds_read_b128 v[34:37], v38 offset:16384
	ds_read_b128 v[38:41], v38 offset:24576
	v_bitop3_b32 v48, v58, v46, 32 bitop3:0xde
	v_add3_u32 v52, v48, v56, s1
	ds_read_b128 v[48:51], v52 offset:16384
	ds_read_b128 v[52:55], v52 offset:24576
	s_waitcnt lgkmcnt(3)
	v_mfma_f32_32x32x16_bf16 v[78:93], v[34:37], v[182:185], 0
	s_waitcnt lgkmcnt(2)
	v_mfma_f32_32x32x16_bf16 v[62:77], v[38:41], v[182:185], 0
	v_bitop3_b32 v34, v58, v46, 64 bitop3:0xde
	v_add3_u32 v38, v34, v56, s1
	ds_read_b128 v[34:37], v38 offset:24576
	ds_read_b128 v[38:41], v38 offset:16384
	s_waitcnt lgkmcnt(3)
	v_mfma_f32_32x32x16_bf16 v[78:93], v[48:51], v[186:189], v[78:93]
	s_waitcnt lgkmcnt(2)
	v_mfma_f32_32x32x16_bf16 v[62:77], v[52:55], v[186:189], v[62:77]
	v_bitop3_b32 v48, v58, v46, s60 bitop3:0xde
	v_add3_u32 v52, v48, v56, s1
	ds_read_b128 v[48:51], v52 offset:16384
	ds_read_b128 v[52:55], v52 offset:24576
	s_waitcnt lgkmcnt(2)
	v_mfma_f32_32x32x16_bf16 v[78:93], v[38:41], v[158:161], v[78:93]
	v_mfma_f32_32x32x16_bf16 v[62:77], v[34:37], v[158:161], v[62:77]
	s_movk_i32 s0, 0x80
	v_bitop3_b32 v34, v58, v46, s0 bitop3:0xde
	v_add3_u32 v38, v34, v56, s1
	ds_read_b128 v[34:37], v38 offset:24576
	ds_read_b128 v[38:41], v38 offset:16384
	s_waitcnt lgkmcnt(3)
	v_mfma_f32_32x32x16_bf16 v[78:93], v[48:51], v[162:165], v[78:93]
	s_waitcnt lgkmcnt(2)
	v_mfma_f32_32x32x16_bf16 v[62:77], v[52:55], v[162:165], v[62:77]
	s_movk_i32 s0, 0xa0
	v_bitop3_b32 v48, v58, v46, s0 bitop3:0xde
	v_add3_u32 v52, v48, v56, s1
	ds_read_b128 v[48:51], v52 offset:16384
	ds_read_b128 v[52:55], v52 offset:24576
	s_waitcnt lgkmcnt(2)
	v_mfma_f32_32x32x16_bf16 v[78:93], v[38:41], v[166:169], v[78:93]
	v_mfma_f32_32x32x16_bf16 v[62:77], v[34:37], v[166:169], v[62:77]
	s_movk_i32 s0, 0xc0
	v_bitop3_b32 v34, v58, v46, s0 bitop3:0xde
	v_add3_u32 v38, v34, v56, s1
	ds_read_b128 v[34:37], v38 offset:24576
	ds_read_b128 v[38:41], v38 offset:16384
	s_waitcnt lgkmcnt(3)
	v_mfma_f32_32x32x16_bf16 v[78:93], v[48:51], v[170:173], v[78:93]
	s_waitcnt lgkmcnt(2)
	v_mfma_f32_32x32x16_bf16 v[62:77], v[52:55], v[170:173], v[62:77]
	s_movk_i32 s0, 0xe0
	v_bitop3_b32 v46, v57, v46, s0 bitop3:0xce
	v_add3_u32 v46, v46, v56, s1
	ds_read_b128 v[48:51], v46 offset:16384
	ds_read_b128 v[52:55], v46 offset:24576
	s_waitcnt lgkmcnt(2)
	v_mfma_f32_32x32x16_bf16 v[78:93], v[38:41], v[174:177], v[78:93]
	v_mfma_f32_32x32x16_bf16 v[62:77], v[34:37], v[174:177], v[62:77]
	s_waitcnt lgkmcnt(1)
	v_mfma_f32_32x32x16_bf16 v[78:93], v[48:51], v[178:181], v[78:93]
	s_waitcnt lgkmcnt(0)
	v_mfma_f32_32x32x16_bf16 v[62:77], v[52:55], v[178:181], v[62:77]
	s_branch .LBB0_1842
.LBB0_1865:
	s_waitcnt vmcnt(0)
	s_bitcmp1_b32 s101, 31
	s_cbranch_scc0 .Lcn_snone_n1x
	s_and_b32 s14, s101, 0x7fffffff
	s_sub_u32 s14, s14, 1
	s_mul_i32 s15, s14, 0x2493
	s_lshr_b32 s15, s15, 16
	s_mul_i32 s67, s15, 7
	s_sub_u32 s67, s14, s67
	s_lshl_b32 s67, s67, 11
	s_add_u32 s67, s67, s100
	s_cmp_ge_u32 s15, 16
	s_cbranch_scc1 .Lcn_dn_n1xd
	s_lshr_b32 vcc_lo, s67, 5
	s_mul_i32 vcc_lo, vcc_lo, 0x2493
	s_lshr_b32 vcc_lo, vcc_lo, 16
	s_mul_i32 vcc_hi, vcc_lo, 0xe0
	s_sub_u32 vcc_hi, s67, vcc_hi
	s_and_b32 s67, s15, 1
	s_lshr_b32 s15, s15, 1
	s_mul_i32 s14, s15, 0x1c00000
	s_add_u32 s14, s14, 0x4a000000
	s_lshr_b32 s15, vcc_hi, 2
	s_lshl_b32 s15, s15, 8
	s_lshl_b32 s67, s67, 7
	s_add_u32 s15, s15, s67
	s_and_b32 s67, vcc_hi, 3
	s_lshl_b32 s67, s67, 5
	s_add_u32 s15, s15, s67
	s_lshl_b32 s15, s15, 11
	s_add_u32 s14, s14, s15
	s_lshl_b32 s15, vcc_lo, 5
	s_add_u32 s14, s14, s15
	v_readlane_b32 s32, v255, 52
	v_readlane_b32 s33, v255, 53
	s_add_u32 s32, s32, s14
	s_addc_u32 s33, s33, 0
	s_mov_b32 s1, 1
	s_branch .Lcn_dd_n1xd

; __device__ __forceinline__ void p0_weights(const Args& a, LAS unsigned char* lds) {
;     ...
;         if (r < 2 * I_IN) { const int l = r / I_IN; r -= l * I_IN; W = a.in[I_WIN] + (size_t)l * D * INW; w.K = D; w.N = INW; w.dst = a.ws + WS_WIN_T + (size_t)l * PW * D * 2; w.kind = 1; }
;         else if ((r -= 2 * I_IN) < 2 * I_OUT) { const int l = r / I_OUT; r -= l * I_OUT; W = a.in[I_WOUT] + (size_t)l * D * D; w.K = D; w.N = D; w.dst = a.ws + WS_WOUT_T + (size_t)l * D * D * 2; }
;         else if ((r -= 2 * I_OUT) < 2 * I_FG) { const int up = r / I_FG; r -= up * I_FG; W = a.in[up ? I_FWU : I_FWG]; w.K = D; w.N = DFF; w.dst = a.ws + WS_FGU_T; w.kind = 2 + up; w.f8 = FFN8_GU; w.scale = F8_WGU; }
;         else if ((r -= 2 * I_FG) < I_FD) { W = a.in[I_FWD]; w.K = DFF; w.N = D; w.dst = a.ws + WS_FD_T; w.f8 = FFN8_DN; w.scale = F8_FD; }
;         else if ((r -= I_FD) < 16 * I_MG) { const int up = r / (8 * I_MG); r -= up * 8 * I_MG; const int e = r / I_MG; r -= e * I_MG; W = a.in[up ? I_MWU : I_MWG] + (size_t)e * D * DFE; w.K = D; w.N = DFE;
;             w.dst = a.ws + WS_MGU_T + (size_t)e * 2 * DFE * D * (MOE_FP8 ? 1 : 2); w.kind = 2 + up; w.f8 = MOE_FP8; w.scale = F8_WGU; }
;         else { r -= 16 * I_MG; const int e = r / I_MD; r -= e * I_MD; W = a.in[I_MWD] + (size_t)e * DFE * D; w.K = DFE; w.N = D; w.dst = a.ws + WS_MD_T + (size_t)e * D * DFE * (MOE_FP8 ? 1 : 2); w.f8 = MOE_FP8; w.scale = F8_WD; }
;         const int nblk = (w.N + 31) >> 5, kb = r / nblk, nb = r - kb * nblk;
;         w.k0 = 128 * kb + 16 * (lane >> 3); w.n = 32 * nb + 4 * (lane & 7); w.valid = w.n < w.N; w.src = W + (size_t)w.k0 * w.N + w.n;
.LBB0_1880:
.Lcn_left:
	s_and_b32 s8, s101, 0x7fffffff
	s_cmp_ge_u32 s8, 168
	s_cbranch_scc1 .Lcn_leftdone
	s_and_b32 s8, s101, 0x7fffffff
	s_cmp_ge_u32 s8, 168
	s_cbranch_scc1 .Lcn_ldum_lf
	s_and_b32 s8, s101, 0x7fffffff
	s_mul_i32 s9, s8, 0x2493
	s_lshr_b32 s9, s9, 16
	s_mul_i32 s10, s9, 7
	s_sub_u32 s10, s8, s10
	s_lshl_b32 s10, s10, 11
	s_add_u32 s10, s10, s100
	s_cmp_ge_u32 s9, 16
	s_cbranch_scc1 .Lcn_dn_lfs
	s_lshr_b32 s11, s10, 5
	s_mul_i32 s11, s11, 0x2493
	s_lshr_b32 s11, s11, 16
	s_mul_i32 s12, s11, 0xe0
	s_sub_u32 s12, s10, s12
	s_and_b32 s10, s9, 1
	s_lshr_b32 s9, s9, 1
	s_mul_i32 s8, s9, 0x3800000
	s_mul_i32 s9, s11, 0xe0000
	s_add_u32 s8, s8, s9
	s_lshl_b32 s9, s12, 7
	s_add_u32 s8, s8, s9
	v_readlane_b32 s32, v255, 46
	v_readlane_b32 s33, v255, 47
	s_cmp_eq_u32 s10, 0
	s_cselect_b32 s32, s98, s32
	s_cselect_b32 s33, s99, s33
	s_add_u32 s32, s32, s8
	s_addc_u32 s33, s33, 0
	s_mov_b32 s1, 1
	s_branch .Lcn_dd_lfs
.Lcn_dn_lfs:
	s_sub_u32 s9, s9, 16
	s_lshr_b32 s11, s10, 6
	s_and_b32 s12, s10, 63
	s_mul_i32 s8, s9, 0x3800000
	s_lshl_b32 s9, s11, 18
	s_add_u32 s8, s8, s9
	s_lshl_b32 s9, s12, 7
	s_add_u32 s8, s8, s9
	v_readlane_b32 s32, v255, 48
	v_readlane_b32 s33, v255, 49
	s_add_u32 s32, s32, s8
	s_addc_u32 s33, s33, 0
	s_mov_b32 s1, 2

; __device__ __forceinline__ unsigned pk4_fp8(float a, float b, float c, float d) { int p = __builtin_amdgcn_cvt_pk_fp8_f32(a, b, 0, false); p = __builtin_amdgcn_cvt_pk_fp8_f32(c, d, p, true); return (unsigned)p; }
; __device__ __forceinline__ void xcd_barrier(const XcdBarrier& b) {
;     asm volatile("s_waitcnt vmcnt(0)" ::: "memory");
;     __syncthreads();
;     if (threadIdx.x == 0) {
;         unsigned* bar = b.bar;
;         __builtin_amdgcn_s_waitcnt(0);
;         unsigned nloc = b.st[0], nx = b.st[1];
;         if (nloc == 0u) { xcd_barrier_complete(bar, b.x, nloc, nx); b.st[0] = nloc; b.st[1] = nx; }
; __device__ __forceinline__ void witem_store(const WItem& w, const f32x4 (&v)[16]) {
;     if (!w.valid) return;
;     if (w.f8) {
; #pragma unroll
;         for (int j = 0; j < 4; ++j) { u32x4 o; const float sc = w.scale;
;             o.x = pk4_fp8(v[0][j] * sc, v[1][j] * sc, v[2][j] * sc, v[3][j] * sc); o.y = pk4_fp8(v[4][j] * sc, v[5][j] * sc, v[6][j] * sc, v[7][j] * sc);
;             o.z = pk4_fp8(v[8][j] * sc, v[9][j] * sc, v[10][j] * sc, v[11][j] * sc); o.w = pk4_fp8(v[12][j] * sc, v[13][j] * sc, v[14][j] * sc, v[15][j] * sc);
;             *(u32x4*)(w.dst + (size_t)witem_row(w.kind, w.n + j) * w.K + w.k0) = o; }
.Lcn_lgo_lf:
	s_movk_i32 s8, 0x2000
	s_cmp_eq_u32 s1, 1
	s_cselect_b32 s8, 0x7000, s8
	v_and_b32_e32 v220, 63, v0
	v_and_b32_e32 v253, 7, v220
	v_lshrrev_b32_e32 v220, 3, v220
	v_lshlrev_b32_e32 v220, 2, v220
	v_lshlrev_b32_e32 v221, 4, v253
	v_lshlrev_b32_e32 v253, 2, v253
	v_mad_u32_u24 v254, v220, s8, v221
	global_load_dwordx4 v[212:215], v254, s[32:33] nt
	s_add_u32 s32, s32, s8
	s_addc_u32 s33, s33, 0
	global_load_dwordx4 v[216:219], v254, s[32:33] nt
	s_add_u32 s32, s32, s8
	s_addc_u32 s33, s33, 0
	global_load_dwordx4 v[224:227], v254, s[32:33] nt
	s_add_u32 s32, s32, s8
	s_addc_u32 s33, s33, 0
	global_load_dwordx2 v[220:221], v254, s[32:33] offset:0 nt
	global_load_dword v253, v254, s[32:33] offset:8 nt
	global_load_dword v254, v254, s[32:33] offset:12 nt
	s_waitcnt vmcnt(0)
	s_bitcmp1_b32 s101, 31
	s_cbranch_scc0 .Lcn_snone_lf
	s_and_b32 s8, s101, 0x7fffffff
	s_sub_u32 s8, s8, 1
	s_mul_i32 s9, s8, 0x2493
	s_lshr_b32 s9, s9, 16
	s_mul_i32 s10, s9, 7
	s_sub_u32 s10, s8, s10
	s_lshl_b32 s10, s10, 11
	s_add_u32 s10, s10, s100
	s_cmp_ge_u32 s9, 16
	s_cbranch_scc1 .Lcn_dn_lfd
	s_lshr_b32 s11, s10, 5
	s_mul_i32 s11, s11, 0x2493
	s_lshr_b32 s11, s11, 16
	s_mul_i32 s12, s11, 0xe0
	s_sub_u32 s12, s10, s12
	s_and_b32 s10, s9, 1
	s_lshr_b32 s9, s9, 1
	s_mul_i32 s8, s9, 0x1c00000
	s_add_u32 s8, s8, 0x4a000000
	s_lshr_b32 s9, s12, 2
	s_lshl_b32 s9, s9, 8
	s_lshl_b32 s10, s10, 7
	s_add_u32 s9, s9, s10
	s_and_b32 s10, s12, 3
	s_lshl_b32 s10, s10, 5
	s_add_u32 s9, s9, s10
	s_lshl_b32 s9, s9, 11
	s_add_u32 s8, s8, s9
	s_lshl_b32 s9, s11, 5
	s_add_u32 s8, s8, s9
	v_readlane_b32 s32, v255, 52
	v_readlane_b32 s33, v255, 53
	s_add_u32 s32, s32, s8
	s_addc_u32 s33, s33, 0
	s_mov_b32 s1, 1
	s_branch .Lcn_dd_lfd
.Lcn_dn_lfd:
	s_sub_u32 s9, s9, 16
	s_lshr_b32 s11, s10, 6
	s_and_b32 s12, s10, 63
	s_mul_i32 s8, s9, 0xe00000
	s_add_u32 s8, s8, 0x66000000
	s_mul_i32 s9, s12, 0x38000
	s_add_u32 s8, s8, s9
	s_lshl_b32 s9, s11, 5
	s_add_u32 s8, s8, s9
	v_readlane_b32 s32, v255, 52
	v_readlane_b32 s33, v255, 53
	s_add_u32 s32, s32, s8
	s_addc_u32 s33, s33, 0
	s_mov_b32 s1, 2
.Lcn_dd_lfd:
	s_bitset0_b32 s101, 31
	s_mov_b32 s0, 0x42000000
	s_movk_i32 s8, 0x800
	s_cmp_eq_u32 s1, 2
	s_cselect_b32 s0, 0x43000000, s0
	s_cselect_b32 s8, 0x1c00, s8
	v_mul_f32_e32 v212, s0, v212
	v_mul_f32_e32 v213, s0, v213
	v_mul_f32_e32 v214, s0, v214
	v_mul_f32_e32 v215, s0, v215
	v_mul_f32_e32 v216, s0, v216
	v_mul_f32_e32 v217, s0, v217
	v_mul_f32_e32 v218, s0, v218
	v_mul_f32_e32 v219, s0, v219
	v_mul_f32_e32 v224, s0, v224
	v_mul_f32_e32 v225, s0, v225
	v_mul_f32_e32 v226, s0, v226
	v_mul_f32_e32 v227, s0, v227
	v_mul_f32_e32 v220, s0, v220
	v_mul_f32_e32 v221, s0, v221
	v_mul_f32_e32 v253, s0, v253
	v_mul_f32_e32 v254, s0, v254
	v_cvt_pk_fp8_f32 v212, v212, v216
	v_cvt_pk_fp8_f32 v213, v213, v217
	v_cvt_pk_fp8_f32 v214, v214, v218
	v_cvt_pk_fp8_f32 v215, v215, v219
	v_cvt_pk_fp8_f32 v212, v224, v220 op_sel:[0,0,1]
	v_cvt_pk_fp8_f32 v213, v225, v221 op_sel:[0,0,1]
	v_cvt_pk_fp8_f32 v214, v226, v253 op_sel:[0,0,1]
	v_cvt_pk_fp8_f32 v215, v227, v254 op_sel:[0,0,1]
	v_and_b32_e32 v216, 63, v0
	v_and_b32_e32 v218, 7, v216
	v_lshrrev_b32_e32 v216, 3, v216
	v_lshlrev_b32_e32 v216, 2, v216
	v_lshlrev_b32_e32 v217, 4, v218
	v_lshlrev_b32_e32 v218, 2, v218
	v_mad_u32_u24 v217, v218, s8, v216
	global_store_dword v217, v212, s[32:33] nt
	v_add_u32_e32 v216, s8, v217
	global_store_dword v216, v213, s[32:33] nt
	v_add_u32_e32 v218, s8, v216
	global_store_dword v218, v214, s[32:33] nt
	v_add_u32_e32 v219, s8, v218
	global_store_dword v219, v215, s[32:33] nt
.Lcn_snone_lf:
	s_branch .Lcn_left
.Lcn_leftdone:
	s_cmp_gt_i32 s79, 17
	s_cselect_b64 s[0:1], -1, 0
	s_and_b64 s[0:1], s[6:7], s[0:1]
	s_andn2_b64 vcc, exec, s[0:1]
	s_cbranch_vccnz .LBB0_1934
	s_waitcnt vmcnt(0)
	s_waitcnt vmcnt(0) lgkmcnt(0)
	s_barrier
	s_mov_b64 s[0:1], exec
	v_readlane_b32 s2, v255, 10
	v_readlane_b32 s3, v255, 11
	s_and_b64 s[2:3], s[0:1], s[2:3]
	s_mov_b64 exec, s[2:3]
	s_cbranch_execz .LBB0_1933
	s_add_i32 s2, 0, 0x24420
	v_mov_b32_e32 v1, s2
	s_waitcnt vmcnt(0) expcnt(0) lgkmcnt(0)
	ds_read_b32 v3, v1
	s_add_i32 s2, 0, 0x24424
	v_mov_b32_e32 v1, s2
	ds_read_b32 v1, v1
	s_waitcnt lgkmcnt(1)
	v_cmp_ne_u32_e32 vcc, 0, v3
	s_cbranch_vccnz .LBB0_1897
	v_readlane_b32 s2, v255, 1
	v_readlane_b32 s3, v255, 2
	s_load_dwordx2 s[8:9], s[2:3], 0xf0
	s_load_dword s7, s[2:3], 0xf8
	s_add_u32 s2, s66, 0x4200
	s_addc_u32 s3, s67, 0
	s_add_u32 s6, s66, 0x4400
	s_waitcnt lgkmcnt(0)
	s_mul_i32 s33, s9, s8
	s_mul_i32 s33, s33, s7
	s_addc_u32 s7, s67, 0
	s_add_u32 s8, s66, 0x4500
	s_addc_u32 s9, s67, 0
	s_add_u32 s10, s66, 0x4600
	s_addc_u32 s11, s67, 0
	s_add_u32 s12, s66, 0x4700
	s_addc_u32 s13, s67, 0
	s_add_u32 s14, s66, 0x4800
	s_addc_u32 s15, s67, 0
	s_add_u32 s16, s66, 0x4900
	s_addc_u32 s17, s67, 0
	s_add_u32 s18, s66, 0x4a00
	s_addc_u32 s19, s67, 0
	s_add_u32 s20, s66, 0x4b00
	s_addc_u32 s21, s67, 0
	s_add_u32 s22, s66, 0x4c00
	s_addc_u32 s23, s67, 0
	s_add_u32 s24, s66, 0x4d00
	s_addc_u32 s25, s67, 0
	s_add_u32 s26, s66, 0x4e00
	s_addc_u32 s27, s67, 0
	s_add_u32 s28, s66, 0x4f00
	s_addc_u32 s29, s67, 0
	s_add_u32 s30, s66, 0x5000
	s_addc_u32 s31, s67, 0
	s_add_u32 s34, s66, 0x5100
	s_addc_u32 s35, s67, 0
	s_add_u32 s36, s66, 0x5200
	s_addc_u32 s37, s67, 0
	s_add_u32 s38, s66, 0x5300
	s_addc_u32 s39, s67, 0
	s_mov_b32 s46, 1
	v_mov_b32_e32 v17, 0
	s_branch .LBB0_1885
